# light workgroups (bid>=216) convert 32 MoE-down fp8 tiles each in their idle unit slot at the end of FFN-up; in-proj L1 hook range shortened accordingly
# baseline (speedup 1.0000x reference)
; #define PG8_LAS __attribute__((address_space(3)))
; #define LAS __attribute__((address_space(3)))
; __device__ __forceinline__ KA ka_get() { KA p = (KA)__builtin_amdgcn_kernarg_segment_ptr(); asm volatile("" : "+s"(p)); return p; }
; #define CV_LOAD(j, R) do { ConvTile c_; if (CV_VALID(j) && CV_DEC(CV_TILE(j), c_)) conv_load(c_.W, c_.N, c_.k0, c_.n0, wave, lane, R); } while (0)
; template <int NSLOT, bool MOE> __device__ __forceinline__ void conv_burst(const ConvHook& h, int bid, PG8_LAS unsigned char* T_, int tid) {
;     KA A = ka_get(); const int lane = tid & 63, wave = __builtin_amdgcn_readfirstlane(tid >> 6); LAS unsigned char* T = (LAS unsigned char*)T_;
;     const int p0 = (h.t0 >> 1) + bid, p1 = h.t1 >> 1;
;     ...
;     if constexpr (NSLOT == 4) {
;         f32x4 R0[8], R1[8], R2[8], R3[8];
;         CV_LOAD(0, R0); CV_LOAD(1, R1); CV_LOAD(2, R2);
; __device__ __forceinline__ void ph_inproj(LAS unsigned char* lds, unsigned char* ws, int l, int bid, int tid) {
;     pg8::Gemm g{(const pg8::bf16_t*)(ws + WS_XN), (const pg8::bf16_t*)(ws + WS_WIN) + (size_t)l * NP * D, MR, NP, D};
;     pg8::MixOrder<NP / 256, D / 64, 1, D, 12, 10, true> S{l ? 32 : NMT, bid, l, l ? 24 : 0, pg8::ConvHook{l ? CT_FFNUP_HI : CT_P0A_HI, l ? CT_INPROJ1_HI : CT_INPROJ0_HI, bid & 1}};
;     pg8::EpiP E{ws};
;     pg8::gemm_phase<pg8::EpiP, decltype(S), true, true>(lds + RING_OFF, g, S, E, tid);
; }
.LBB0_744:
	v_lshrrev_b32_e32 v18, 1, v150
	v_readlane_b32 s12, v253, 62
	v_and_b32_e32 v18, 24, v18
	v_readlane_b32 s13, v253, 63
	v_and_b32_e32 v17, 15, v150
	v_lshlrev_b32_e32 v19, 1, v18
	s_and_b64 s[12:13], s[12:13], exec
	s_movk_i32 s0, 0x2646
	s_movk_i32 s5, 0x10ca
	v_lshl_or_b32 v151, s1, 6, v17
	v_lshl_or_b32 v17, v17, 6, v19
	v_lshlrev_b32_e32 v19, 2, v150
	s_cselect_b32 s0, 0x800, s0
	s_cselect_b32 s60, s5, 0x2f80
	s_lshl_b32 s1, s1, 13
	v_and_b32_e32 v19, 32, v19
	v_bitop3_b32 v20, v17, s1, v19 bitop3:0xde
	s_lshl_b32 s1, s8, 5
	s_and_b32 s5, s17, 1
	s_and_b32 s1, s1, 0x60
	s_add_i32 m0, s46, 0x18000
	v_lshl_add_u64 v[6:7], v[6:7], 0, s[34:35]
	v_writelane_b32 v254, s5, 30
	s_lshl_b32 s5, s1, 7
	s_waitcnt vmcnt(2)
	s_barrier
	global_load_lds_dwordx4 v[6:7], off
	v_lshl_add_u64 v[4:5], v[4:5], 0, s[34:35]
	s_add_i32 m0, s46, 0x1a000
	s_add_i32 s54, s46, 0x8000
	s_add_i32 s55, s46, 0xa000
	global_load_lds_dwordx4 v[4:5], off
	v_lshl_add_u64 v[2:3], v[2:3], 0, s[34:35]
	s_mov_b32 m0, s54
	s_add_u32 s8, s6, 0x80080
	global_load_lds_dwordx4 v[2:3], off
	v_lshl_add_u64 v[2:3], v[8:9], 0, s[34:35]
	s_mov_b32 m0, s55
	s_addc_u32 s9, s7, 0
	global_load_lds_dwordx4 v[2:3], off
	s_add_i32 m0, s46, 0x1c000
	v_lshl_add_u64 v[2:3], s[8:9], 0, v[136:137]
	global_load_lds_dwordx4 v[2:3], off
	s_add_i32 m0, s46, 0x1e000
	v_lshl_add_u64 v[2:3], s[8:9], 0, v[140:141]
	s_cmpk_lt_u32 s2, 0x100
	global_load_lds_dwordx4 v[2:3], off
	s_cselect_b64 s[70:71], -1, 0
	s_add_u32 s22, s10, 0x39600000
	v_and_b32_e32 v2, 63, v150
	v_readlane_b32 s2, v253, 55
	v_bitop3_b32 v152, s5, v17, v19 bitop3:0xf6
	s_addc_u32 s23, s11, 0
	v_lshlrev_b32_e32 v153, 2, v2
	v_lshl_add_u32 v155, v2, 8, s2
	v_bitop3_b32 v2, v16, 48, v150 bitop3:0x48
	s_and_b32 s5, s26, 4
	v_add_u32_e32 v157, s2, v2
	s_lshr_b32 s2, s26, 3
	v_writelane_b32 v254, s5, 31
	v_writelane_b32 v254, s2, 32
	s_add_i32 s2, s2, 1
	s_add_i32 s28, s17, s0
	s_cmp_lt_i32 s28, s60
	v_writelane_b32 v254, s2, 33
	s_cselect_b64 s[8:9], -1, 0
	s_lshl_b32 s5, s28, 1
	v_writelane_b32 v254, s8, 34
	s_cmpk_lt_i32 s28, 0x2400
	v_lshlrev_b32_e32 v2, 15, v10
	v_writelane_b32 v254, s9, 35
	s_cselect_b64 s[8:9], -1, 0
	v_writelane_b32 v254, s8, 36
	s_cmpk_gt_i32 s28, 0x23ff
	v_lshlrev_b32_e32 v3, 1, v150
	v_writelane_b32 v254, s9, 37
	s_cselect_b64 s[8:9], -1, 0
	v_writelane_b32 v254, s8, 38
	s_cmpk_gt_u32 s5, 0x63ff
	v_and_b32_e32 v2, 0xffff0000, v2
	v_writelane_b32 v254, s9, 39
	s_cselect_b64 s[8:9], -1, 0
	s_add_i32 s2, s5, 0xb800
	s_bfe_u32 s10, s2, 0x90007
	s_mulk_i32 s10, 0x2493
	v_writelane_b32 v254, s8, 40
	s_lshr_b32 s10, s10, 16
	s_add_i32 s13, s5, 0xbff
	v_writelane_b32 v254, s9, 41
	s_mov_b32 s8, s10
	s_mulk_i32 s10, 0x380
	s_sub_i32 s2, s2, s10
	s_and_b32 s2, s2, 0xfffe
	v_writelane_b32 v254, s8, 42
	s_lshl_b32 s10, s2, 3
	s_lshl_b32 s2, s2, 7
	v_writelane_b32 v254, s9, 43
	s_and_b32 s8, s10, 0x1f80
	v_writelane_b32 v254, s8, 44
	s_and_b32 s2, s2, 0x700
	v_writelane_b32 v254, s2, 45
	s_add_i32 s2, s5, 0xfffff000
	s_mul_hi_i32 s10, s2, 0x92492493
	s_add_i32 s10, s10, s2
	s_lshr_b32 s11, s10, 31
	s_ashr_i32 s10, s10, 12
	s_add_i32 s10, s10, s11
	s_mulk_i32 s10, 0x1c00
	s_sub_i32 s10, s2, s10
	s_sext_i32_i16 s2, s10
	s_mulk_i32 s2, 0x4925
	s_lshr_b32 s11, s2, 31
	s_ashr_i32 s2, s2, 24
	s_add_i32 s2, s2, s11
	s_mul_i32 s11, s2, 0x380
	s_sub_i32 s10, s10, s11
	s_sext_i32_i16 s11, s10
	s_lshr_b32 s12, s11, 1
	s_cmpk_lt_u32 s13, 0x37ff
	s_cselect_b32 s8, s63, 0xd8
	s_bfe_i64 s[18:19], s[2:3], 0x100000
	s_ashr_i32 s2, s11, 1
	s_mulk_i32 s2, 0x4925
	s_lshr_b32 s11, s2, 31
	s_ashr_i32 s2, s2, 19
	s_add_i32 s2, s2, s11
	s_sext_i32_i16 s11, s2
	s_lshl_b32 s10, s10, 6
	v_writelane_b32 v254, s18, 46
	s_lshl_b32 s11, s11, 7
	s_and_b32 s10, s10, 64
	v_writelane_b32 v254, s19, 47
	s_or_b32 s10, s11, s10
	v_writelane_b32 v254, s10, 48
	s_add_i32 s10, s5, 0xb801
	s_bfe_u32 s11, s10, 0x90007
	s_mulk_i32 s11, 0x2493
	s_mul_i32 s2, s2, 28
	s_lshr_b32 s11, s11, 16
	s_sub_i32 s2, s12, s2
	s_mul_i32 s12, s11, 0x380
	s_sub_i32 s10, s10, s12
	s_and_b32 s10, s10, 0xffff
	s_lshl_b32 s12, s10, 3
	s_lshl_b32 s13, s10, 6
	s_and_b32 s12, s12, 0x1f80
	s_and_b32 s13, s13, 64
	s_or_b32 s12, s12, s13
	s_add_i32 s13, s5, 0xfffff001
	s_mul_hi_i32 s15, s13, 0x92492493
	s_add_i32 s15, s15, s13
	s_lshr_b32 s16, s15, 31
	s_ashr_i32 s15, s15, 12
	s_add_i32 s15, s15, s16
	s_mulk_i32 s15, 0x1c00
	s_sub_i32 s13, s13, s15
	s_sext_i32_i16 s15, s13
	s_mulk_i32 s15, 0x4925
	s_lshr_b32 s16, s15, 31
	s_ashr_i32 s15, s15, 24
; #define CV_LOAD(j, R) do { ConvTile c_; if (CV_VALID(j) && CV_DEC(CV_TILE(j), c_)) conv_load(c_.W, c_.N, c_.k0, c_.n0, wave, lane, R); } while (0)
; __device__ __forceinline__ bool conv_decode_moe(KA A, int t, ConvTile& c) {
;     unsigned char* ws = A->ws; c.f8 = 1; c.K = D; c.N = FFE; t -= 4096;
;     if (t < 14336) { const int hf = t / 7168, r2 = t % 7168, e = r2 / 896, r = r2 % 896, hk = r & 1, q = r >> 1; c.W = (hf ? A->in[I_MWU] : A->in[I_MWG]) + (size_t)e * D * FFE; c.WT = ws + WS_MUP + (size_t)e * 2 * FFE * D; c.k0 = 128 * (q / 28) + 64 * hk; c.n0 = 256 * (q % 28); c.kind = 2 + hf; return true; } t -= 14336;
;     if (t >= 7168) return false;
;     { const int e = t / 896, r = t % 896, hk = r & 1, q = r >> 1; c.W = A->in[I_MWD] + (size_t)e * FFE * D; c.WT = ws + WS_MDN + (size_t)e * D * FFE; c.K = FFE; c.N = D; c.k0 = 128 * (q >> 3) + 64 * hk; c.n0 = 256 * (q & 7); c.kind = 0; return true; }
; template <int NSLOT, bool MOE> __device__ __forceinline__ void conv_burst(const ConvHook& h, int bid, PG8_LAS unsigned char* T_, int tid) {
;     ...
;     const int p0 = (h.t0 >> 1) + bid, p1 = h.t1 >> 1;
;     ...
;     if constexpr (NSLOT == 4) {
;         f32x4 R0[8], R1[8], R2[8], R3[8];
;         CV_LOAD(0, R0); CV_LOAD(1, R1); CV_LOAD(2, R2);
	s_add_i32 s15, s15, s16
	s_mul_i32 s16, s15, 0x380
	s_sext_i32_i16 s2, s2
	s_sub_i32 s13, s13, s16
	s_lshl_b32 s2, s2, 8
	s_lshl_b32 s10, s10, 7
	s_sext_i32_i16 s16, s13
	v_writelane_b32 v254, s2, 49
	s_or_b32 s2, s5, 1
	s_and_b32 s10, s10, 0x700
	s_lshr_b32 s18, s16, 1
	s_addk_i32 s5, 0xc00
	s_cmpk_lt_u32 s5, 0x37ff
	s_cselect_b32 s5, s63, 0xd8
	s_ashr_i32 s16, s16, 1
	s_mulk_i32 s16, 0x4925
	s_lshr_b32 s19, s16, 31
	s_ashr_i32 s16, s16, 19
	s_add_i32 s16, s16, s19
	s_sext_i32_i16 s19, s16
	s_mul_i32 s16, s16, 28
	s_lshl_b32 s13, s13, 6
	s_sub_i32 s16, s18, s16
	s_lshl_b32 s19, s19, 7
	s_and_b32 s13, s13, 64
	s_sext_i32_i16 s16, s16
	s_or_b32 s13, s19, s13
	s_lshl_b32 s16, s16, 8
	s_add_i32 s18, s28, 0x100
	s_cmp_lt_i32 s18, s60
	s_cselect_b64 s[20:21], -1, 0
	s_lshl_b32 s18, s18, 1
	v_writelane_b32 v254, s20, 50
	s_cmpk_lt_i32 s28, 0x2300
	s_mov_b32 s9, 0
	v_writelane_b32 v254, s21, 51
	s_cselect_b64 s[20:21], -1, 0
	v_writelane_b32 v254, s20, 52
	s_cmpk_gt_i32 s28, 0x22ff
	s_mov_b32 s37, s9
	v_writelane_b32 v254, s21, 53
	s_cselect_b64 s[20:21], -1, 0
	v_writelane_b32 v254, s20, 54
	s_cmpk_lt_u32 s18, 0x6400
	v_and_b32_e32 v154, 6, v3
	v_writelane_b32 v254, s21, 55
	s_cselect_b64 s[20:21], -1, 0
	v_writelane_b32 v254, s20, 56
	s_add_i32 s19, s18, 0xb800
	v_lshl_add_u32 v2, v11, 12, v2
	v_writelane_b32 v254, s21, 57
	s_bfe_u32 s20, s19, 0x90007
	s_mulk_i32 s20, 0x2493
	s_lshr_b32 s24, s20, 16
	s_mov_b32 s20, s24
	v_writelane_b32 v254, s20, 58
	v_and_b32_e32 v3, 1, v10
	v_lshl_or_b32 v2, v3, 6, v2
	v_writelane_b32 v254, s21, 59
	s_mul_i32 s20, s24, 0x380
	s_sub_i32 s19, s19, s20
	s_and_b32 s19, s19, 0xfffe
	s_lshl_b32 s20, s19, 3
	s_and_b32 s20, s20, 0x1f80
	s_lshl_b32 s19, s19, 7
	v_writelane_b32 v254, s20, 60
	s_and_b32 s19, s19, 0x700
	v_writelane_b32 v254, s19, 61
	s_add_i32 s19, s18, 0xfffff000
	s_mul_hi_i32 s20, s19, 0x92492493
	s_add_i32 s20, s20, s19
	s_lshr_b32 s21, s20, 31
	s_ashr_i32 s20, s20, 12
	s_add_i32 s20, s20, s21
	s_mulk_i32 s20, 0x1c00
	s_sub_i32 s19, s19, s20
	s_sext_i32_i16 s20, s19
	s_mulk_i32 s20, 0x4925
	s_lshr_b32 s21, s20, 31
	s_ashr_i32 s20, s20, 24
	s_add_i32 s24, s20, s21
	s_mov_b32 s20, s24
	v_writelane_b32 v254, s20, 62
	s_addk_i32 s18, 0xbff
	v_lshl_add_u32 v144, v12, 1, v2
	v_writelane_b32 v254, s21, 63
	s_mul_i32 s20, s24, 0x380
	s_sub_i32 s19, s19, s20
	s_sext_i32_i16 s20, s19
	s_lshr_b32 s21, s20, 1
	s_cmpk_lt_u32 s18, 0x37ff
	s_cselect_b32 s36, s63, 0xd8
	s_ashr_i32 s18, s20, 1
	s_mulk_i32 s18, 0x4925
	s_lshr_b32 s20, s18, 31
	s_ashr_i32 s18, s18, 19
	s_add_i32 s18, s18, s20
	s_lshl_b32 s20, s18, 7
	s_lshl_b32 s19, s19, 6
	s_mul_i32 s18, s18, 28
	s_and_b32 s19, s19, 64
	s_sub_i32 s18, s21, s18
	s_or_b32 s19, s20, s19
	s_sext_i32_i16 s18, s18
	v_writelane_b32 v255, s19, 0
	s_lshl_b32 s18, s18, 8
	v_writelane_b32 v255, s18, 1
	s_cmpk_lt_i32 s2, 0x4800
	v_writelane_b32 v255, s36, 2
	s_cselect_b32 s2, s5, 0xe0
	v_lshlrev_b32_e32 v2, 15, v13
	v_writelane_b32 v255, s37, 3
	v_writelane_b32 v255, s2, 4
	s_sext_i32_i16 s2, s15
	s_cselect_b32 s2, s2, s11
	s_mul_hi_i32 s5, s2, 0x3800000
	v_writelane_b32 v255, s5, 5
	s_mul_i32 s2, s2, 0x3800000
	v_writelane_b32 v255, s2, 6
	s_cselect_b32 s5, s13, s12
	v_writelane_b32 v255, s5, 7
	s_movk_i32 s5, 0x1c00
	s_cselect_b32 s5, s5, 0x800
	s_cselect_b32 s2, s16, s10
	s_lshl_b32 s10, s5, 3
	s_mov_b32 s11, s25
	v_writelane_b32 v255, s10, 8
	v_and_b32_e32 v2, 0xffff0000, v2
	s_lshl_b32 s21, s0, 1
	v_writelane_b32 v255, s11, 9
	s_lshl_b32 s10, s5, 4
	s_mov_b32 s11, s25
	v_writelane_b32 v255, s10, 10
	s_lshl_b32 s0, s17, 1
	s_waitcnt vmcnt(6)
	v_ashrrev_i32_e32 v156, 2, v150
	v_writelane_b32 v255, s11, 11
	s_mul_i32 s10, s5, 24
	s_mov_b32 s11, s25
	v_writelane_b32 v255, s10, 12
	v_lshl_add_u32 v2, v14, 12, v2
	v_and_b32_e32 v3, 1, v13
	v_writelane_b32 v255, s11, 13
	v_writelane_b32 v255, s5, 14
	s_lshl_b32 s10, s5, 2
	s_mov_b32 s11, s25
	v_writelane_b32 v255, s10, 15
	v_add_u32_e32 v160, 0x80, v156
	v_or_b32_e32 v142, s2, v153
	v_writelane_b32 v255, s11, 16
	v_writelane_b32 v255, s0, 17
	v_lshl_or_b32 v2, v3, 6, v2
	v_writelane_b32 v255, s8, 18
	v_and_b32_e32 v158, 48, v16
	v_lshlrev_b32_e32 v159, 6, v156
	v_lshlrev_b32_e32 v161, 6, v160
	v_cmp_gt_i32_e64 s[38:39], s5, v142
	v_ashrrev_i32_e32 v143, 31, v142
	v_or_b32_e32 v162, s1, v18
	v_mov_b32_e32 v145, v130
	v_lshl_add_u32 v146, v15, 1, v2
	v_mov_b32_e32 v147, v130
	v_add_u32_e32 v163, 0, v20
	v_writelane_b32 v255, s9, 19
	s_mov_b32 s0, s9
	s_barrier
	s_branch .LBB0_747

; #define GAS __attribute__((address_space(1)))
; __device__ __forceinline__ void conv_load(const float* W, int N, int k0, int n0, int wave, int lane, f32x4 (&r)[8]) {
;     const int n = n0 + 4 * lane; const bool ok = n < N;
;     const float* p = W + (size_t)(k0 + 8 * wave) * N + n;
; #pragma unroll
;     for (int i = 0; i < 8; ++i) r[i] = ok ? __builtin_nontemporal_load((const GAS f32x4*)(p + (size_t)i * N)) : (f32x4){0.f, 0.f, 0.f, 0.f};
; }
; __device__ __forceinline__ bool conv_decode_moe(KA A, int t, ConvTile& c) {
;     unsigned char* ws = A->ws; c.f8 = 1; c.K = D; c.N = FFE; t -= 4096;
;     if (t < 14336) { const int hf = t / 7168, r2 = t % 7168, e = r2 / 896, r = r2 % 896, hk = r & 1, q = r >> 1; c.W = (hf ? A->in[I_MWU] : A->in[I_MWG]) + (size_t)e * D * FFE; c.WT = ws + WS_MUP + (size_t)e * 2 * FFE * D; c.k0 = 128 * (q / 28) + 64 * hk; c.n0 = 256 * (q % 28); c.kind = 2 + hf; return true; } t -= 14336;
;     if (t >= 7168) return false;
;     { const int e = t / 896, r = t % 896, hk = r & 1, q = r >> 1; c.W = A->in[I_MWD] + (size_t)e * FFE * D; c.WT = ws + WS_MDN + (size_t)e * D * FFE; c.K = FFE; c.N = D; c.k0 = 128 * (q >> 3) + 64 * hk; c.n0 = 256 * (q & 7); c.kind = 0; return true; }
.LBB0_2448:
	v_readlane_b32 s101, v254, 2
	s_nop 3
	s_cmpk_lt_u32 s101, 0xd8
	s_cbranch_scc1 .Lic_skip_ffnup
	v_writelane_b32 v255, s4, 25
	v_writelane_b32 v255, s5, 26
	v_writelane_b32 v255, s6, 27
	v_writelane_b32 v255, s7, 28
	v_writelane_b32 v255, s8, 29
	v_writelane_b32 v255, s9, 30
	v_writelane_b32 v255, s10, 31
	v_writelane_b32 v255, s11, 32
	v_writelane_b32 v255, s12, 33
	v_writelane_b32 v255, s13, 34
	v_writelane_b32 v255, s14, 35
	v_writelane_b32 v255, s15, 36
	v_writelane_b32 v255, s16, 37
	v_writelane_b32 v255, s17, 38
	v_writelane_b32 v255, s18, 39
	v_writelane_b32 v255, s19, 40
	v_writelane_b32 v255, s20, 41
	v_writelane_b32 v255, s21, 42
	v_writelane_b32 v255, s22, 43
	v_writelane_b32 v255, s23, 44
	v_writelane_b32 v255, s24, 45
	v_writelane_b32 v255, s25, 46
	v_writelane_b32 v255, s26, 47
	v_writelane_b32 v255, s27, 48
	v_writelane_b32 v255, s28, 49
	v_writelane_b32 v255, s29, 50
	v_writelane_b32 v255, s30, 51
	v_writelane_b32 v255, s31, 52
	v_writelane_b32 v255, s32, 53
	v_writelane_b32 v255, s33, 54
	v_writelane_b32 v255, s34, 55
	v_writelane_b32 v255, s35, 56
	v_writelane_b32 v255, s36, 57
	v_writelane_b32 v255, s37, 58
	v_writelane_b32 v255, s38, 59
	v_writelane_b32 v255, s39, 60
	v_readlane_b32 s24, v254, 3
	v_readlane_b32 s25, v254, 4
	s_nop 4
	s_load_dwordx2 s[26:27], s[24:25], 0xf8
	s_load_dwordx2 s[38:39], s[24:25], 0xe0
	v_readfirstlane_b32 s28, v0
	s_nop 3
	s_lshr_b32 s28, s28, 6
	v_and_b32_e32 v160, 63, v0
	v_and_b32_e32 v161, 3, v0
	v_lshrrev_b32_e32 v162, 2, v0
	v_and_b32_e32 v164, 3, v160
	v_lshlrev_b32_e32 v164, 1, v164
	v_xor_b32_e32 v164, s28, v164
	v_lshlrev_b32_e32 v163, 8, v160
	v_lshl_add_u32 v163, v164, 3, v163
	v_add_u32_e32 v163, 0x20000, v163
	v_lshrrev_b32_e32 v164, 2, v162
	v_and_b32_e32 v164, 3, v164
	v_xor_b32_e32 v164, v161, v164
	v_lshlrev_b32_e32 v164, 4, v164
	v_lshl_add_u32 v164, v162, 6, v164
	v_add_u32_e32 v164, 0x20000, v164
	v_lshlrev_b32_e32 v165, 4, v160
	v_lshlrev_b32_e32 v166, 7, v162
	v_lshl_add_u32 v166, v161, 4, v166
	v_mov_b32_e32 v158, 0x43e00000
	v_mov_b32_e32 v159, 0
	s_sub_i32 s15, s101, 0xd8
	s_add_i32 s15, s15, 0x2f80
	s_mov_b32 s101, 0xc3e00000
	s_waitcnt lgkmcnt(0)
	s_lshl_b32 s14, s15, 1
	s_sub_i32 s14, s14, 0x4800
	s_mul_hi_u32 s16, s14, 0x92492493
	s_lshr_b32 s16, s16, 9
	s_mul_i32 s17, s16, 0x380
	s_sub_i32 s17, s14, s17
	s_lshr_b32 s17, s17, 1
	s_mul_i32 s18, s16, 0x3800000
	s_mul_hi_u32 s19, s16, 0x3800000
	s_add_u32 s4, s38, s18
	s_addc_u32 s5, s39, s19
	s_lshr_b32 s18, s17, 3
	s_lshl_b32 s19, s18, 7
	s_lshl_b32 s20, s28, 3
	s_add_i32 s19, s19, s20
	s_lshl_b32 s19, s19, 11
	s_and_b32 s20, s17, 7
	s_lshl_b32 s21, s20, 8
	s_add_i32 s19, s19, s21
	s_lshl_b32 s19, s19, 2
	s_add_u32 s4, s4, s19
	s_addc_u32 s5, s5, 0
	s_mul_i32 s21, s16, 0xe00000
	s_add_u32 s6, s26, 0x25000000
	s_addc_u32 s7, s27, 0
	s_add_u32 s6, s6, s21
	s_addc_u32 s7, s7, 0
	s_mul_i32 s20, s20, 56
	s_add_i32 s20, s20, s18
	s_lshl_b32 s20, s20, 15
	s_add_u32 s6, s6, s20
	s_addc_u32 s7, s7, 0
	s_addk_i32 s15, 0x28
	s_mov_b32 s30, s6
	s_mov_b32 s31, s7
	global_load_dwordx4 v[2:5], v165, s[4:5] nt
	s_add_u32 s4, s4, 0x2000
	s_addc_u32 s5, s5, 0
	global_load_dwordx4 v[6:9], v165, s[4:5] nt
	s_add_u32 s4, s4, 0x2000
	s_addc_u32 s5, s5, 0
	global_load_dwordx4 v[10:13], v165, s[4:5] nt
	s_add_u32 s4, s4, 0x2000
	s_addc_u32 s5, s5, 0
	global_load_dwordx4 v[14:17], v165, s[4:5] nt
	s_add_u32 s4, s4, 0x2000
	s_addc_u32 s5, s5, 0
	global_load_dwordx4 v[18:21], v165, s[4:5] nt
	s_add_u32 s4, s4, 0x2000
	s_addc_u32 s5, s5, 0
	global_load_dwordx4 v[22:25], v165, s[4:5] nt
	s_add_u32 s4, s4, 0x2000
	s_addc_u32 s5, s5, 0
	global_load_dwordx4 v[26:29], v165, s[4:5] nt
	s_add_u32 s4, s4, 0x2000
	s_addc_u32 s5, s5, 0
	global_load_dwordx4 v[30:33], v165, s[4:5] nt
	s_add_u32 s4, s4, 0x72000
	s_addc_u32 s5, s5, 0
	s_add_u32 s32, s30, 64
	s_addc_u32 s33, s31, 0
	global_load_dwordx4 v[34:37], v165, s[4:5] nt
	s_add_u32 s4, s4, 0x2000
	s_addc_u32 s5, s5, 0
	global_load_dwordx4 v[38:41], v165, s[4:5] nt
	s_add_u32 s4, s4, 0x2000
	s_addc_u32 s5, s5, 0
	global_load_dwordx4 v[42:45], v165, s[4:5] nt
	s_add_u32 s4, s4, 0x2000
	s_addc_u32 s5, s5, 0
	global_load_dwordx4 v[46:49], v165, s[4:5] nt
	s_add_u32 s4, s4, 0x2000
	s_addc_u32 s5, s5, 0
	global_load_dwordx4 v[50:53], v165, s[4:5] nt
	s_add_u32 s4, s4, 0x2000
	s_addc_u32 s5, s5, 0
	global_load_dwordx4 v[54:57], v165, s[4:5] nt
	s_add_u32 s4, s4, 0x2000
	s_addc_u32 s5, s5, 0
	global_load_dwordx4 v[58:61], v165, s[4:5] nt
	s_add_u32 s4, s4, 0x2000
	s_addc_u32 s5, s5, 0
	global_load_dwordx4 v[62:65], v165, s[4:5] nt
	s_lshl_b32 s14, s15, 1
	s_sub_i32 s14, s14, 0x4800
	s_mul_hi_u32 s16, s14, 0x92492493
	s_lshr_b32 s16, s16, 9
	s_mul_i32 s17, s16, 0x380
	s_sub_i32 s17, s14, s17
	s_lshr_b32 s17, s17, 1
	s_mul_i32 s18, s16, 0x3800000
	s_mul_hi_u32 s19, s16, 0x3800000
	s_add_u32 s4, s38, s18
	s_addc_u32 s5, s39, s19
	s_lshr_b32 s18, s17, 3
	s_lshl_b32 s19, s18, 7
	s_lshl_b32 s20, s28, 3
	s_add_i32 s19, s19, s20
	s_lshl_b32 s19, s19, 11
	s_and_b32 s20, s17, 7
	s_lshl_b32 s21, s20, 8
	s_add_i32 s19, s19, s21
	s_lshl_b32 s19, s19, 2
	s_add_u32 s4, s4, s19
	s_addc_u32 s5, s5, 0
	s_mul_i32 s21, s16, 0xe00000
	s_add_u32 s6, s26, 0x25000000
	s_addc_u32 s7, s27, 0
	s_add_u32 s6, s6, s21
	s_addc_u32 s7, s7, 0
	s_mul_i32 s20, s20, 56
	s_add_i32 s20, s20, s18
	s_lshl_b32 s20, s20, 15
	s_add_u32 s6, s6, s20
	s_addc_u32 s7, s7, 0
	s_addk_i32 s15, 0x28
	s_mov_b32 s34, s6
	s_mov_b32 s35, s7
	global_load_dwordx4 v[66:69], v165, s[4:5] nt
	s_add_u32 s4, s4, 0x2000
	s_addc_u32 s5, s5, 0
	global_load_dwordx4 v[70:73], v165, s[4:5] nt
	s_add_u32 s4, s4, 0x2000
	s_addc_u32 s5, s5, 0
	global_load_dwordx4 v[74:77], v165, s[4:5] nt
	s_add_u32 s4, s4, 0x2000
	s_addc_u32 s5, s5, 0
	global_load_dwordx4 v[78:81], v165, s[4:5] nt
	s_add_u32 s4, s4, 0x2000
	s_addc_u32 s5, s5, 0
	global_load_dwordx4 v[82:85], v165, s[4:5] nt
	s_add_u32 s4, s4, 0x2000
	s_addc_u32 s5, s5, 0
	global_load_dwordx4 v[86:89], v165, s[4:5] nt
	s_add_u32 s4, s4, 0x2000
	s_addc_u32 s5, s5, 0
	global_load_dwordx4 v[90:93], v165, s[4:5] nt
	s_add_u32 s4, s4, 0x2000
	s_addc_u32 s5, s5, 0
	global_load_dwordx4 v[94:97], v165, s[4:5] nt
	s_mov_b32 s29, 7
; #define GAS __attribute__((address_space(1)))
; #define LAS __attribute__((address_space(3)))
; #define LDS_BARRIER() do { asm volatile("s_waitcnt lgkmcnt(0)" ::: "memory"); __builtin_amdgcn_s_barrier(); asm volatile("" ::: "memory"); } while (0)
; __device__ __forceinline__ unsigned pk4_fp8(float a, float b, float c, float d) {
;     a = __builtin_amdgcn_fmed3f(a, -448.f, 448.f); b = __builtin_amdgcn_fmed3f(b, -448.f, 448.f); c = __builtin_amdgcn_fmed3f(c, -448.f, 448.f); d = __builtin_amdgcn_fmed3f(d, -448.f, 448.f);
;     int w = 0; w = __builtin_amdgcn_cvt_pk_fp8_f32(a, b, w, false); w = __builtin_amdgcn_cvt_pk_fp8_f32(c, d, w, true); return (unsigned)w; }
; template <class RowMap>
; __device__ __forceinline__ void conv_store_fp8(const f32x4 (&r)[8], unsigned char* WT, int Kbytes, int k0bytes, int n0, const RowMap rm, LAS unsigned char* T, int tid, int wave, int lane) {
;     const int s = 2 * (lane & 3);
; #pragma unroll
;     for (int j = 0; j < 4; ++j) { const unsigned lo = pk4_fp8(r[0][j] * W8_SCALE, r[1][j] * W8_SCALE, r[2][j] * W8_SCALE, r[3][j] * W8_SCALE), hi = pk4_fp8(r[4][j] * W8_SCALE, r[5][j] * W8_SCALE, r[6][j] * W8_SCALE, r[7][j] * W8_SCALE);
;         *(LAS unsigned long long*)(T + (4 * lane + j) * 64 + 8 * (wave ^ s)) = (unsigned long long)lo | ((unsigned long long)hi << 32); }
;     LDS_BARRIER();
;     const int c16 = tid & 3, rr = tid >> 2;
; #pragma unroll
;     for (int q = 0; q < 2; ++q) { const int row = rr + 128 * q; const v4u v = *(const LAS v4u*)(T + row * 64 + 16 * (c16 ^ ((row >> 2) & 3)));
;         const int dr = rm(n0 + row); if (dr >= 0) *(GAS v4u*)(WT + (unsigned)((((dr >> 8) * (Kbytes >> 7) + (k0bytes >> 7)) << 15) + ((dr & 255) << 7) + (k0bytes & 127) + 16 * c16)) = v; }
;     LDS_BARRIER();
; }
.Lic_body_ffnup:
	s_add_u32 s4, s4, 0x72000
	s_addc_u32 s5, s5, 0
	s_add_u32 s36, s34, 64
	s_addc_u32 s37, s35, 0
	global_load_dwordx4 v[98:101], v165, s[4:5] nt
	s_add_u32 s4, s4, 0x2000
	s_addc_u32 s5, s5, 0
	global_load_dwordx4 v[102:105], v165, s[4:5] nt
	s_add_u32 s4, s4, 0x2000
	s_addc_u32 s5, s5, 0
	global_load_dwordx4 v[106:109], v165, s[4:5] nt
	s_add_u32 s4, s4, 0x2000
	s_addc_u32 s5, s5, 0
	global_load_dwordx4 v[110:113], v165, s[4:5] nt
	s_add_u32 s4, s4, 0x2000
	s_addc_u32 s5, s5, 0
	global_load_dwordx4 v[114:117], v165, s[4:5] nt
	s_add_u32 s4, s4, 0x2000
	s_addc_u32 s5, s5, 0
	global_load_dwordx4 v[118:121], v165, s[4:5] nt
	s_add_u32 s4, s4, 0x2000
	s_addc_u32 s5, s5, 0
	global_load_dwordx4 v[122:125], v165, s[4:5] nt
	s_add_u32 s4, s4, 0x2000
	s_addc_u32 s5, s5, 0
	global_load_dwordx4 v[126:129], v165, s[4:5] nt
	s_waitcnt vmcnt(24)
	v_mov_b32_e32 v140, v159
	v_mul_f32_e32 v148, 0x42800000, v2
	v_mul_f32_e32 v149, 0x42800000, v6
	v_med3_f32 v148, v148, s101, v158
	v_med3_f32 v149, v149, s101, v158
	v_cvt_pk_fp8_f32 v140, v148, v149
	v_mul_f32_e32 v148, 0x42800000, v10
	v_mul_f32_e32 v149, 0x42800000, v14
	v_med3_f32 v148, v148, s101, v158
	v_med3_f32 v149, v149, s101, v158
	v_cvt_pk_fp8_f32 v140, v148, v149 op_sel:[0,0,1]
	v_mov_b32_e32 v141, v159
	v_mul_f32_e32 v148, 0x42800000, v18
	v_mul_f32_e32 v149, 0x42800000, v22
	v_med3_f32 v148, v148, s101, v158
	v_med3_f32 v149, v149, s101, v158
	v_cvt_pk_fp8_f32 v141, v148, v149
	v_mul_f32_e32 v148, 0x42800000, v26
	v_mul_f32_e32 v149, 0x42800000, v30
	v_med3_f32 v148, v148, s101, v158
	v_med3_f32 v149, v149, s101, v158
	v_cvt_pk_fp8_f32 v141, v148, v149 op_sel:[0,0,1]
	v_mov_b32_e32 v142, v159
	v_mul_f32_e32 v148, 0x42800000, v3
	v_mul_f32_e32 v149, 0x42800000, v7
	v_med3_f32 v148, v148, s101, v158
	v_med3_f32 v149, v149, s101, v158
	v_cvt_pk_fp8_f32 v142, v148, v149
	v_mul_f32_e32 v148, 0x42800000, v11
	v_mul_f32_e32 v149, 0x42800000, v15
	v_med3_f32 v148, v148, s101, v158
	v_med3_f32 v149, v149, s101, v158
	v_cvt_pk_fp8_f32 v142, v148, v149 op_sel:[0,0,1]
	v_mov_b32_e32 v143, v159
	v_mul_f32_e32 v148, 0x42800000, v19
	v_mul_f32_e32 v149, 0x42800000, v23
	v_med3_f32 v148, v148, s101, v158
	v_med3_f32 v149, v149, s101, v158
	v_cvt_pk_fp8_f32 v143, v148, v149
	v_mul_f32_e32 v148, 0x42800000, v27
	v_mul_f32_e32 v149, 0x42800000, v31
	v_med3_f32 v148, v148, s101, v158
	v_med3_f32 v149, v149, s101, v158
	v_cvt_pk_fp8_f32 v143, v148, v149 op_sel:[0,0,1]
	v_mov_b32_e32 v144, v159
	v_mul_f32_e32 v148, 0x42800000, v4
	v_mul_f32_e32 v149, 0x42800000, v8
	v_med3_f32 v148, v148, s101, v158
	v_med3_f32 v149, v149, s101, v158
	v_cvt_pk_fp8_f32 v144, v148, v149
	v_mul_f32_e32 v148, 0x42800000, v12
	v_mul_f32_e32 v149, 0x42800000, v16
	v_med3_f32 v148, v148, s101, v158
	v_med3_f32 v149, v149, s101, v158
	v_cvt_pk_fp8_f32 v144, v148, v149 op_sel:[0,0,1]
	v_mov_b32_e32 v145, v159
	v_mul_f32_e32 v148, 0x42800000, v20
	v_mul_f32_e32 v149, 0x42800000, v24
	v_med3_f32 v148, v148, s101, v158
	v_med3_f32 v149, v149, s101, v158
	v_cvt_pk_fp8_f32 v145, v148, v149
	v_mul_f32_e32 v148, 0x42800000, v28
	v_mul_f32_e32 v149, 0x42800000, v32
	v_med3_f32 v148, v148, s101, v158
	v_med3_f32 v149, v149, s101, v158
	v_cvt_pk_fp8_f32 v145, v148, v149 op_sel:[0,0,1]
	v_mov_b32_e32 v146, v159
	v_mul_f32_e32 v148, 0x42800000, v5
	v_mul_f32_e32 v149, 0x42800000, v9
	v_med3_f32 v148, v148, s101, v158
	v_med3_f32 v149, v149, s101, v158
	v_cvt_pk_fp8_f32 v146, v148, v149
	v_mul_f32_e32 v148, 0x42800000, v13
	v_mul_f32_e32 v149, 0x42800000, v17
	v_med3_f32 v148, v148, s101, v158
	v_med3_f32 v149, v149, s101, v158
	v_cvt_pk_fp8_f32 v146, v148, v149 op_sel:[0,0,1]
	v_mov_b32_e32 v147, v159
	v_mul_f32_e32 v148, 0x42800000, v21
	v_mul_f32_e32 v149, 0x42800000, v25
	v_med3_f32 v148, v148, s101, v158
	v_med3_f32 v149, v149, s101, v158
	v_cvt_pk_fp8_f32 v147, v148, v149
	v_mul_f32_e32 v148, 0x42800000, v29
	v_mul_f32_e32 v149, 0x42800000, v33
	v_med3_f32 v148, v148, s101, v158
	v_med3_f32 v149, v149, s101, v158
	v_cvt_pk_fp8_f32 v147, v148, v149 op_sel:[0,0,1]
	ds_write_b64 v163, v[140:141]
	ds_write_b64 v163, v[142:143] offset:64
	ds_write_b64 v163, v[144:145] offset:128
	ds_write_b64 v163, v[146:147] offset:192
	s_waitcnt lgkmcnt(0)
	s_barrier
	ds_read_b128 v[150:153], v164
	ds_read_b128 v[154:157], v164 offset:8192
	s_add_u32 s22, s30, 0x4000
	s_addc_u32 s23, s31, 0
	s_waitcnt lgkmcnt(1)
	global_store_dwordx4 v166, v[150:153], s[30:31]
	s_waitcnt lgkmcnt(0)
	global_store_dwordx4 v166, v[154:157], s[22:23]
	s_barrier
; #define GAS __attribute__((address_space(1)))
; #define LAS __attribute__((address_space(3)))
; #define LDS_BARRIER() do { asm volatile("s_waitcnt lgkmcnt(0)" ::: "memory"); __builtin_amdgcn_s_barrier(); asm volatile("" ::: "memory"); } while (0)
; template <class RowMap>
; __device__ __forceinline__ void conv_store_fp8(const f32x4 (&r)[8], unsigned char* WT, int Kbytes, int k0bytes, int n0, const RowMap rm, LAS unsigned char* T, int tid, int wave, int lane) {
;     const int s = 2 * (lane & 3);
; #pragma unroll
;     for (int j = 0; j < 4; ++j) { const unsigned lo = pk4_fp8(r[0][j] * W8_SCALE, r[1][j] * W8_SCALE, r[2][j] * W8_SCALE, r[3][j] * W8_SCALE), hi = pk4_fp8(r[4][j] * W8_SCALE, r[5][j] * W8_SCALE, r[6][j] * W8_SCALE, r[7][j] * W8_SCALE);
;         *(LAS unsigned long long*)(T + (4 * lane + j) * 64 + 8 * (wave ^ s)) = (unsigned long long)lo | ((unsigned long long)hi << 32); }
;     LDS_BARRIER();
;     const int c16 = tid & 3, rr = tid >> 2;
; #pragma unroll
;     for (int q = 0; q < 2; ++q) { const int row = rr + 128 * q; const v4u v = *(const LAS v4u*)(T + row * 64 + 16 * (c16 ^ ((row >> 2) & 3)));
;         const int dr = rm(n0 + row); if (dr >= 0) *(GAS v4u*)(WT + (unsigned)((((dr >> 8) * (Kbytes >> 7) + (k0bytes >> 7)) << 15) + ((dr & 255) << 7) + (k0bytes & 127) + 16 * c16)) = v; }
;     LDS_BARRIER();
; }
; __device__ __forceinline__ bool conv_decode_moe(KA A, int t, ConvTile& c) {
;     unsigned char* ws = A->ws; c.f8 = 1; c.K = D; c.N = FFE; t -= 4096;
;     if (t < 14336) { const int hf = t / 7168, r2 = t % 7168, e = r2 / 896, r = r2 % 896, hk = r & 1, q = r >> 1; c.W = (hf ? A->in[I_MWU] : A->in[I_MWG]) + (size_t)e * D * FFE; c.WT = ws + WS_MUP + (size_t)e * 2 * FFE * D; c.k0 = 128 * (q / 28) + 64 * hk; c.n0 = 256 * (q % 28); c.kind = 2 + hf; return true; } t -= 14336;
;     if (t >= 7168) return false;
;     { const int e = t / 896, r = t % 896, hk = r & 1, q = r >> 1; c.W = A->in[I_MWD] + (size_t)e * FFE * D; c.WT = ws + WS_MDN + (size_t)e * D * FFE; c.K = FFE; c.N = D; c.k0 = 128 * (q >> 3) + 64 * hk; c.n0 = 256 * (q & 7); c.kind = 0; return true; }
	s_lshl_b32 s14, s15, 1
	s_sub_i32 s14, s14, 0x4800
	s_mul_hi_u32 s16, s14, 0x92492493
	s_lshr_b32 s16, s16, 9
	s_mul_i32 s17, s16, 0x380
	s_sub_i32 s17, s14, s17
	s_lshr_b32 s17, s17, 1
	s_mul_i32 s18, s16, 0x3800000
	s_mul_hi_u32 s19, s16, 0x3800000
	s_add_u32 s4, s38, s18
	s_addc_u32 s5, s39, s19
	s_lshr_b32 s18, s17, 3
	s_lshl_b32 s19, s18, 7
	s_lshl_b32 s20, s28, 3
	s_add_i32 s19, s19, s20
	s_lshl_b32 s19, s19, 11
	s_and_b32 s20, s17, 7
	s_lshl_b32 s21, s20, 8
	s_add_i32 s19, s19, s21
	s_lshl_b32 s19, s19, 2
	s_add_u32 s4, s4, s19
	s_addc_u32 s5, s5, 0
	s_mul_i32 s21, s16, 0xe00000
	s_add_u32 s6, s26, 0x25000000
	s_addc_u32 s7, s27, 0
	s_add_u32 s6, s6, s21
	s_addc_u32 s7, s7, 0
	s_mul_i32 s20, s20, 56
	s_add_i32 s20, s20, s18
	s_lshl_b32 s20, s20, 15
	s_add_u32 s6, s6, s20
	s_addc_u32 s7, s7, 0
	s_addk_i32 s15, 0x28
	s_mov_b32 s30, s6
	s_mov_b32 s31, s7
	global_load_dwordx4 v[2:5], v165, s[4:5] nt
	s_add_u32 s4, s4, 0x2000
	s_addc_u32 s5, s5, 0
	global_load_dwordx4 v[6:9], v165, s[4:5] nt
	s_add_u32 s4, s4, 0x2000
	s_addc_u32 s5, s5, 0
	global_load_dwordx4 v[10:13], v165, s[4:5] nt
	s_add_u32 s4, s4, 0x2000
	s_addc_u32 s5, s5, 0
	global_load_dwordx4 v[14:17], v165, s[4:5] nt
	s_add_u32 s4, s4, 0x2000
	s_addc_u32 s5, s5, 0
	global_load_dwordx4 v[18:21], v165, s[4:5] nt
	s_add_u32 s4, s4, 0x2000
	s_addc_u32 s5, s5, 0
	global_load_dwordx4 v[22:25], v165, s[4:5] nt
	s_add_u32 s4, s4, 0x2000
	s_addc_u32 s5, s5, 0
	global_load_dwordx4 v[26:29], v165, s[4:5] nt
	s_add_u32 s4, s4, 0x2000
	s_addc_u32 s5, s5, 0
	global_load_dwordx4 v[30:33], v165, s[4:5] nt
	s_waitcnt vmcnt(24)
	v_mov_b32_e32 v140, v159
	v_mul_f32_e32 v148, 0x42800000, v34
	v_mul_f32_e32 v149, 0x42800000, v38
	v_med3_f32 v148, v148, s101, v158
	v_med3_f32 v149, v149, s101, v158
	v_cvt_pk_fp8_f32 v140, v148, v149
	v_mul_f32_e32 v148, 0x42800000, v42
	v_mul_f32_e32 v149, 0x42800000, v46
	v_med3_f32 v148, v148, s101, v158
	v_med3_f32 v149, v149, s101, v158
	v_cvt_pk_fp8_f32 v140, v148, v149 op_sel:[0,0,1]
	v_mov_b32_e32 v141, v159
	v_mul_f32_e32 v148, 0x42800000, v50
	v_mul_f32_e32 v149, 0x42800000, v54
	v_med3_f32 v148, v148, s101, v158
	v_med3_f32 v149, v149, s101, v158
	v_cvt_pk_fp8_f32 v141, v148, v149
	v_mul_f32_e32 v148, 0x42800000, v58
	v_mul_f32_e32 v149, 0x42800000, v62
	v_med3_f32 v148, v148, s101, v158
	v_med3_f32 v149, v149, s101, v158
	v_cvt_pk_fp8_f32 v141, v148, v149 op_sel:[0,0,1]
	v_mov_b32_e32 v142, v159
	v_mul_f32_e32 v148, 0x42800000, v35
	v_mul_f32_e32 v149, 0x42800000, v39
	v_med3_f32 v148, v148, s101, v158
	v_med3_f32 v149, v149, s101, v158
	v_cvt_pk_fp8_f32 v142, v148, v149
	v_mul_f32_e32 v148, 0x42800000, v43
	v_mul_f32_e32 v149, 0x42800000, v47
	v_med3_f32 v148, v148, s101, v158
	v_med3_f32 v149, v149, s101, v158
	v_cvt_pk_fp8_f32 v142, v148, v149 op_sel:[0,0,1]
	v_mov_b32_e32 v143, v159
	v_mul_f32_e32 v148, 0x42800000, v51
	v_mul_f32_e32 v149, 0x42800000, v55
	v_med3_f32 v148, v148, s101, v158
	v_med3_f32 v149, v149, s101, v158
	v_cvt_pk_fp8_f32 v143, v148, v149
	v_mul_f32_e32 v148, 0x42800000, v59
	v_mul_f32_e32 v149, 0x42800000, v63
	v_med3_f32 v148, v148, s101, v158
	v_med3_f32 v149, v149, s101, v158
	v_cvt_pk_fp8_f32 v143, v148, v149 op_sel:[0,0,1]
	v_mov_b32_e32 v144, v159
	v_mul_f32_e32 v148, 0x42800000, v36
	v_mul_f32_e32 v149, 0x42800000, v40
	v_med3_f32 v148, v148, s101, v158
	v_med3_f32 v149, v149, s101, v158
	v_cvt_pk_fp8_f32 v144, v148, v149
	v_mul_f32_e32 v148, 0x42800000, v44
	v_mul_f32_e32 v149, 0x42800000, v48
	v_med3_f32 v148, v148, s101, v158
	v_med3_f32 v149, v149, s101, v158
	v_cvt_pk_fp8_f32 v144, v148, v149 op_sel:[0,0,1]
	v_mov_b32_e32 v145, v159
	v_mul_f32_e32 v148, 0x42800000, v52
	v_mul_f32_e32 v149, 0x42800000, v56
	v_med3_f32 v148, v148, s101, v158
	v_med3_f32 v149, v149, s101, v158
	v_cvt_pk_fp8_f32 v145, v148, v149
	v_mul_f32_e32 v148, 0x42800000, v60
	v_mul_f32_e32 v149, 0x42800000, v64
	v_med3_f32 v148, v148, s101, v158
	v_med3_f32 v149, v149, s101, v158
	v_cvt_pk_fp8_f32 v145, v148, v149 op_sel:[0,0,1]
	v_mov_b32_e32 v146, v159
	v_mul_f32_e32 v148, 0x42800000, v37
	v_mul_f32_e32 v149, 0x42800000, v41
	v_med3_f32 v148, v148, s101, v158
	v_med3_f32 v149, v149, s101, v158
	v_cvt_pk_fp8_f32 v146, v148, v149
	v_mul_f32_e32 v148, 0x42800000, v45
	v_mul_f32_e32 v149, 0x42800000, v49
	v_med3_f32 v148, v148, s101, v158
	v_med3_f32 v149, v149, s101, v158
	v_cvt_pk_fp8_f32 v146, v148, v149 op_sel:[0,0,1]
	v_mov_b32_e32 v147, v159
	v_mul_f32_e32 v148, 0x42800000, v53
	v_mul_f32_e32 v149, 0x42800000, v57
	v_med3_f32 v148, v148, s101, v158
	v_med3_f32 v149, v149, s101, v158
	v_cvt_pk_fp8_f32 v147, v148, v149
	v_mul_f32_e32 v148, 0x42800000, v61
	v_mul_f32_e32 v149, 0x42800000, v65
	v_med3_f32 v148, v148, s101, v158
	v_med3_f32 v149, v149, s101, v158
	v_cvt_pk_fp8_f32 v147, v148, v149 op_sel:[0,0,1]
	ds_write_b64 v163, v[140:141]
	ds_write_b64 v163, v[142:143] offset:64
	ds_write_b64 v163, v[144:145] offset:128
	ds_write_b64 v163, v[146:147] offset:192
	s_waitcnt lgkmcnt(0)
	s_barrier
	ds_read_b128 v[150:153], v164
	ds_read_b128 v[154:157], v164 offset:8192
	s_add_u32 s22, s32, 0x4000
	s_addc_u32 s23, s33, 0
	s_waitcnt lgkmcnt(1)
	global_store_dwordx4 v166, v[150:153], s[32:33]
	s_waitcnt lgkmcnt(0)
	global_store_dwordx4 v166, v[154:157], s[22:23]
	s_barrier
; #define GAS __attribute__((address_space(1)))
; #define LAS __attribute__((address_space(3)))
; #define LDS_BARRIER() do { asm volatile("s_waitcnt lgkmcnt(0)" ::: "memory"); __builtin_amdgcn_s_barrier(); asm volatile("" ::: "memory"); } while (0)
; __device__ __forceinline__ void conv_load(const float* W, int N, int k0, int n0, int wave, int lane, f32x4 (&r)[8]) {
;     const int n = n0 + 4 * lane; const bool ok = n < N;
;     const float* p = W + (size_t)(k0 + 8 * wave) * N + n;
; #pragma unroll
;     for (int i = 0; i < 8; ++i) r[i] = ok ? __builtin_nontemporal_load((const GAS f32x4*)(p + (size_t)i * N)) : (f32x4){0.f, 0.f, 0.f, 0.f};
; }
; template <class RowMap>
; __device__ __forceinline__ void conv_store_fp8(const f32x4 (&r)[8], unsigned char* WT, int Kbytes, int k0bytes, int n0, const RowMap rm, LAS unsigned char* T, int tid, int wave, int lane) {
;     const int s = 2 * (lane & 3);
; #pragma unroll
;     for (int j = 0; j < 4; ++j) { const unsigned lo = pk4_fp8(r[0][j] * W8_SCALE, r[1][j] * W8_SCALE, r[2][j] * W8_SCALE, r[3][j] * W8_SCALE), hi = pk4_fp8(r[4][j] * W8_SCALE, r[5][j] * W8_SCALE, r[6][j] * W8_SCALE, r[7][j] * W8_SCALE);
;         *(LAS unsigned long long*)(T + (4 * lane + j) * 64 + 8 * (wave ^ s)) = (unsigned long long)lo | ((unsigned long long)hi << 32); }
;     LDS_BARRIER();
;     const int c16 = tid & 3, rr = tid >> 2;
; #pragma unroll
;     for (int q = 0; q < 2; ++q) { const int row = rr + 128 * q; const v4u v = *(const LAS v4u*)(T + row * 64 + 16 * (c16 ^ ((row >> 2) & 3)));
;         const int dr = rm(n0 + row); if (dr >= 0) *(GAS v4u*)(WT + (unsigned)((((dr >> 8) * (Kbytes >> 7) + (k0bytes >> 7)) << 15) + ((dr & 255) << 7) + (k0bytes & 127) + 16 * c16)) = v; }
;     LDS_BARRIER();
; }
	s_add_u32 s4, s4, 0x72000
	s_addc_u32 s5, s5, 0
	s_add_u32 s32, s30, 64
	s_addc_u32 s33, s31, 0
	global_load_dwordx4 v[34:37], v165, s[4:5] nt
	s_add_u32 s4, s4, 0x2000
	s_addc_u32 s5, s5, 0
	global_load_dwordx4 v[38:41], v165, s[4:5] nt
	s_add_u32 s4, s4, 0x2000
	s_addc_u32 s5, s5, 0
	global_load_dwordx4 v[42:45], v165, s[4:5] nt
	s_add_u32 s4, s4, 0x2000
	s_addc_u32 s5, s5, 0
	global_load_dwordx4 v[46:49], v165, s[4:5] nt
	s_add_u32 s4, s4, 0x2000
	s_addc_u32 s5, s5, 0
	global_load_dwordx4 v[50:53], v165, s[4:5] nt
	s_add_u32 s4, s4, 0x2000
	s_addc_u32 s5, s5, 0
	global_load_dwordx4 v[54:57], v165, s[4:5] nt
	s_add_u32 s4, s4, 0x2000
	s_addc_u32 s5, s5, 0
	global_load_dwordx4 v[58:61], v165, s[4:5] nt
	s_add_u32 s4, s4, 0x2000
	s_addc_u32 s5, s5, 0
	global_load_dwordx4 v[62:65], v165, s[4:5] nt
	s_waitcnt vmcnt(24)
	v_mov_b32_e32 v140, v159
	v_mul_f32_e32 v148, 0x42800000, v66
	v_mul_f32_e32 v149, 0x42800000, v70
	v_med3_f32 v148, v148, s101, v158
	v_med3_f32 v149, v149, s101, v158
	v_cvt_pk_fp8_f32 v140, v148, v149
	v_mul_f32_e32 v148, 0x42800000, v74
	v_mul_f32_e32 v149, 0x42800000, v78
	v_med3_f32 v148, v148, s101, v158
	v_med3_f32 v149, v149, s101, v158
	v_cvt_pk_fp8_f32 v140, v148, v149 op_sel:[0,0,1]
	v_mov_b32_e32 v141, v159
	v_mul_f32_e32 v148, 0x42800000, v82
	v_mul_f32_e32 v149, 0x42800000, v86
	v_med3_f32 v148, v148, s101, v158
	v_med3_f32 v149, v149, s101, v158
	v_cvt_pk_fp8_f32 v141, v148, v149
	v_mul_f32_e32 v148, 0x42800000, v90
	v_mul_f32_e32 v149, 0x42800000, v94
	v_med3_f32 v148, v148, s101, v158
	v_med3_f32 v149, v149, s101, v158
	v_cvt_pk_fp8_f32 v141, v148, v149 op_sel:[0,0,1]
	v_mov_b32_e32 v142, v159
	v_mul_f32_e32 v148, 0x42800000, v67
	v_mul_f32_e32 v149, 0x42800000, v71
	v_med3_f32 v148, v148, s101, v158
	v_med3_f32 v149, v149, s101, v158
	v_cvt_pk_fp8_f32 v142, v148, v149
	v_mul_f32_e32 v148, 0x42800000, v75
	v_mul_f32_e32 v149, 0x42800000, v79
	v_med3_f32 v148, v148, s101, v158
	v_med3_f32 v149, v149, s101, v158
	v_cvt_pk_fp8_f32 v142, v148, v149 op_sel:[0,0,1]
	v_mov_b32_e32 v143, v159
	v_mul_f32_e32 v148, 0x42800000, v83
	v_mul_f32_e32 v149, 0x42800000, v87
	v_med3_f32 v148, v148, s101, v158
	v_med3_f32 v149, v149, s101, v158
	v_cvt_pk_fp8_f32 v143, v148, v149
	v_mul_f32_e32 v148, 0x42800000, v91
	v_mul_f32_e32 v149, 0x42800000, v95
	v_med3_f32 v148, v148, s101, v158
	v_med3_f32 v149, v149, s101, v158
	v_cvt_pk_fp8_f32 v143, v148, v149 op_sel:[0,0,1]
	v_mov_b32_e32 v144, v159
	v_mul_f32_e32 v148, 0x42800000, v68
	v_mul_f32_e32 v149, 0x42800000, v72
	v_med3_f32 v148, v148, s101, v158
	v_med3_f32 v149, v149, s101, v158
	v_cvt_pk_fp8_f32 v144, v148, v149
	v_mul_f32_e32 v148, 0x42800000, v76
	v_mul_f32_e32 v149, 0x42800000, v80
	v_med3_f32 v148, v148, s101, v158
	v_med3_f32 v149, v149, s101, v158
	v_cvt_pk_fp8_f32 v144, v148, v149 op_sel:[0,0,1]
	v_mov_b32_e32 v145, v159
	v_mul_f32_e32 v148, 0x42800000, v84
	v_mul_f32_e32 v149, 0x42800000, v88
	v_med3_f32 v148, v148, s101, v158
	v_med3_f32 v149, v149, s101, v158
	v_cvt_pk_fp8_f32 v145, v148, v149
	v_mul_f32_e32 v148, 0x42800000, v92
	v_mul_f32_e32 v149, 0x42800000, v96
	v_med3_f32 v148, v148, s101, v158
	v_med3_f32 v149, v149, s101, v158
	v_cvt_pk_fp8_f32 v145, v148, v149 op_sel:[0,0,1]
	v_mov_b32_e32 v146, v159
	v_mul_f32_e32 v148, 0x42800000, v69
	v_mul_f32_e32 v149, 0x42800000, v73
	v_med3_f32 v148, v148, s101, v158
	v_med3_f32 v149, v149, s101, v158
	v_cvt_pk_fp8_f32 v146, v148, v149
	v_mul_f32_e32 v148, 0x42800000, v77
	v_mul_f32_e32 v149, 0x42800000, v81
	v_med3_f32 v148, v148, s101, v158
	v_med3_f32 v149, v149, s101, v158
	v_cvt_pk_fp8_f32 v146, v148, v149 op_sel:[0,0,1]
	v_mov_b32_e32 v147, v159
	v_mul_f32_e32 v148, 0x42800000, v85
	v_mul_f32_e32 v149, 0x42800000, v89
	v_med3_f32 v148, v148, s101, v158
	v_med3_f32 v149, v149, s101, v158
	v_cvt_pk_fp8_f32 v147, v148, v149
	v_mul_f32_e32 v148, 0x42800000, v93
	v_mul_f32_e32 v149, 0x42800000, v97
	v_med3_f32 v148, v148, s101, v158
	v_med3_f32 v149, v149, s101, v158
	v_cvt_pk_fp8_f32 v147, v148, v149 op_sel:[0,0,1]
	ds_write_b64 v163, v[140:141]
	ds_write_b64 v163, v[142:143] offset:64
	ds_write_b64 v163, v[144:145] offset:128
	ds_write_b64 v163, v[146:147] offset:192
	s_waitcnt lgkmcnt(0)
	s_barrier
	ds_read_b128 v[150:153], v164
	ds_read_b128 v[154:157], v164 offset:8192
	s_add_u32 s22, s34, 0x4000
	s_addc_u32 s23, s35, 0
	s_waitcnt lgkmcnt(1)
	global_store_dwordx4 v166, v[150:153], s[34:35]
	s_waitcnt lgkmcnt(0)
	global_store_dwordx4 v166, v[154:157], s[22:23]
	s_barrier
; #define GAS __attribute__((address_space(1)))
; #define LAS __attribute__((address_space(3)))
; #define LDS_BARRIER() do { asm volatile("s_waitcnt lgkmcnt(0)" ::: "memory"); __builtin_amdgcn_s_barrier(); asm volatile("" ::: "memory"); } while (0)
; template <class RowMap>
; __device__ __forceinline__ void conv_store_fp8(const f32x4 (&r)[8], unsigned char* WT, int Kbytes, int k0bytes, int n0, const RowMap rm, LAS unsigned char* T, int tid, int wave, int lane) {
;     const int s = 2 * (lane & 3);
; #pragma unroll
;     for (int j = 0; j < 4; ++j) { const unsigned lo = pk4_fp8(r[0][j] * W8_SCALE, r[1][j] * W8_SCALE, r[2][j] * W8_SCALE, r[3][j] * W8_SCALE), hi = pk4_fp8(r[4][j] * W8_SCALE, r[5][j] * W8_SCALE, r[6][j] * W8_SCALE, r[7][j] * W8_SCALE);
;         *(LAS unsigned long long*)(T + (4 * lane + j) * 64 + 8 * (wave ^ s)) = (unsigned long long)lo | ((unsigned long long)hi << 32); }
;     LDS_BARRIER();
;     const int c16 = tid & 3, rr = tid >> 2;
; #pragma unroll
;     for (int q = 0; q < 2; ++q) { const int row = rr + 128 * q; const v4u v = *(const LAS v4u*)(T + row * 64 + 16 * (c16 ^ ((row >> 2) & 3)));
;         const int dr = rm(n0 + row); if (dr >= 0) *(GAS v4u*)(WT + (unsigned)((((dr >> 8) * (Kbytes >> 7) + (k0bytes >> 7)) << 15) + ((dr & 255) << 7) + (k0bytes & 127) + 16 * c16)) = v; }
;     LDS_BARRIER();
; }
; __device__ __forceinline__ bool conv_decode_moe(KA A, int t, ConvTile& c) {
;     unsigned char* ws = A->ws; c.f8 = 1; c.K = D; c.N = FFE; t -= 4096;
;     if (t < 14336) { const int hf = t / 7168, r2 = t % 7168, e = r2 / 896, r = r2 % 896, hk = r & 1, q = r >> 1; c.W = (hf ? A->in[I_MWU] : A->in[I_MWG]) + (size_t)e * D * FFE; c.WT = ws + WS_MUP + (size_t)e * 2 * FFE * D; c.k0 = 128 * (q / 28) + 64 * hk; c.n0 = 256 * (q % 28); c.kind = 2 + hf; return true; } t -= 14336;
;     if (t >= 7168) return false;
;     { const int e = t / 896, r = t % 896, hk = r & 1, q = r >> 1; c.W = A->in[I_MWD] + (size_t)e * FFE * D; c.WT = ws + WS_MDN + (size_t)e * D * FFE; c.K = FFE; c.N = D; c.k0 = 128 * (q >> 3) + 64 * hk; c.n0 = 256 * (q & 7); c.kind = 0; return true; }
	s_lshl_b32 s14, s15, 1
	s_sub_i32 s14, s14, 0x4800
	s_mul_hi_u32 s16, s14, 0x92492493
	s_lshr_b32 s16, s16, 9
	s_mul_i32 s17, s16, 0x380
	s_sub_i32 s17, s14, s17
	s_lshr_b32 s17, s17, 1
	s_mul_i32 s18, s16, 0x3800000
	s_mul_hi_u32 s19, s16, 0x3800000
	s_add_u32 s4, s38, s18
	s_addc_u32 s5, s39, s19
	s_lshr_b32 s18, s17, 3
	s_lshl_b32 s19, s18, 7
	s_lshl_b32 s20, s28, 3
	s_add_i32 s19, s19, s20
	s_lshl_b32 s19, s19, 11
	s_and_b32 s20, s17, 7
	s_lshl_b32 s21, s20, 8
	s_add_i32 s19, s19, s21
	s_lshl_b32 s19, s19, 2
	s_add_u32 s4, s4, s19
	s_addc_u32 s5, s5, 0
	s_mul_i32 s21, s16, 0xe00000
	s_add_u32 s6, s26, 0x25000000
	s_addc_u32 s7, s27, 0
	s_add_u32 s6, s6, s21
	s_addc_u32 s7, s7, 0
	s_mul_i32 s20, s20, 56
	s_add_i32 s20, s20, s18
	s_lshl_b32 s20, s20, 15
	s_add_u32 s6, s6, s20
	s_addc_u32 s7, s7, 0
	s_addk_i32 s15, 0x28
	s_mov_b32 s34, s6
	s_mov_b32 s35, s7
	global_load_dwordx4 v[66:69], v165, s[4:5] nt
	s_add_u32 s4, s4, 0x2000
	s_addc_u32 s5, s5, 0
	global_load_dwordx4 v[70:73], v165, s[4:5] nt
	s_add_u32 s4, s4, 0x2000
	s_addc_u32 s5, s5, 0
	global_load_dwordx4 v[74:77], v165, s[4:5] nt
	s_add_u32 s4, s4, 0x2000
	s_addc_u32 s5, s5, 0
	global_load_dwordx4 v[78:81], v165, s[4:5] nt
	s_add_u32 s4, s4, 0x2000
	s_addc_u32 s5, s5, 0
	global_load_dwordx4 v[82:85], v165, s[4:5] nt
	s_add_u32 s4, s4, 0x2000
	s_addc_u32 s5, s5, 0
	global_load_dwordx4 v[86:89], v165, s[4:5] nt
	s_add_u32 s4, s4, 0x2000
	s_addc_u32 s5, s5, 0
	global_load_dwordx4 v[90:93], v165, s[4:5] nt
	s_add_u32 s4, s4, 0x2000
	s_addc_u32 s5, s5, 0
	global_load_dwordx4 v[94:97], v165, s[4:5] nt
	s_waitcnt vmcnt(24)
	v_mov_b32_e32 v140, v159
	v_mul_f32_e32 v148, 0x42800000, v98
	v_mul_f32_e32 v149, 0x42800000, v102
	v_med3_f32 v148, v148, s101, v158
	v_med3_f32 v149, v149, s101, v158
	v_cvt_pk_fp8_f32 v140, v148, v149
	v_mul_f32_e32 v148, 0x42800000, v106
	v_mul_f32_e32 v149, 0x42800000, v110
	v_med3_f32 v148, v148, s101, v158
	v_med3_f32 v149, v149, s101, v158
	v_cvt_pk_fp8_f32 v140, v148, v149 op_sel:[0,0,1]
	v_mov_b32_e32 v141, v159
	v_mul_f32_e32 v148, 0x42800000, v114
	v_mul_f32_e32 v149, 0x42800000, v118
	v_med3_f32 v148, v148, s101, v158
	v_med3_f32 v149, v149, s101, v158
	v_cvt_pk_fp8_f32 v141, v148, v149
	v_mul_f32_e32 v148, 0x42800000, v122
	v_mul_f32_e32 v149, 0x42800000, v126
	v_med3_f32 v148, v148, s101, v158
	v_med3_f32 v149, v149, s101, v158
	v_cvt_pk_fp8_f32 v141, v148, v149 op_sel:[0,0,1]
	v_mov_b32_e32 v142, v159
	v_mul_f32_e32 v148, 0x42800000, v99
	v_mul_f32_e32 v149, 0x42800000, v103
	v_med3_f32 v148, v148, s101, v158
	v_med3_f32 v149, v149, s101, v158
	v_cvt_pk_fp8_f32 v142, v148, v149
	v_mul_f32_e32 v148, 0x42800000, v107
	v_mul_f32_e32 v149, 0x42800000, v111
	v_med3_f32 v148, v148, s101, v158
	v_med3_f32 v149, v149, s101, v158
	v_cvt_pk_fp8_f32 v142, v148, v149 op_sel:[0,0,1]
	v_mov_b32_e32 v143, v159
	v_mul_f32_e32 v148, 0x42800000, v115
	v_mul_f32_e32 v149, 0x42800000, v119
	v_med3_f32 v148, v148, s101, v158
	v_med3_f32 v149, v149, s101, v158
	v_cvt_pk_fp8_f32 v143, v148, v149
	v_mul_f32_e32 v148, 0x42800000, v123
	v_mul_f32_e32 v149, 0x42800000, v127
	v_med3_f32 v148, v148, s101, v158
	v_med3_f32 v149, v149, s101, v158
	v_cvt_pk_fp8_f32 v143, v148, v149 op_sel:[0,0,1]
	v_mov_b32_e32 v144, v159
	v_mul_f32_e32 v148, 0x42800000, v100
	v_mul_f32_e32 v149, 0x42800000, v104
	v_med3_f32 v148, v148, s101, v158
	v_med3_f32 v149, v149, s101, v158
	v_cvt_pk_fp8_f32 v144, v148, v149
	v_mul_f32_e32 v148, 0x42800000, v108
	v_mul_f32_e32 v149, 0x42800000, v112
	v_med3_f32 v148, v148, s101, v158
	v_med3_f32 v149, v149, s101, v158
	v_cvt_pk_fp8_f32 v144, v148, v149 op_sel:[0,0,1]
	v_mov_b32_e32 v145, v159
	v_mul_f32_e32 v148, 0x42800000, v116
	v_mul_f32_e32 v149, 0x42800000, v120
	v_med3_f32 v148, v148, s101, v158
	v_med3_f32 v149, v149, s101, v158
	v_cvt_pk_fp8_f32 v145, v148, v149
	v_mul_f32_e32 v148, 0x42800000, v124
	v_mul_f32_e32 v149, 0x42800000, v128
	v_med3_f32 v148, v148, s101, v158
	v_med3_f32 v149, v149, s101, v158
	v_cvt_pk_fp8_f32 v145, v148, v149 op_sel:[0,0,1]
	v_mov_b32_e32 v146, v159
	v_mul_f32_e32 v148, 0x42800000, v101
	v_mul_f32_e32 v149, 0x42800000, v105
	v_med3_f32 v148, v148, s101, v158
	v_med3_f32 v149, v149, s101, v158
	v_cvt_pk_fp8_f32 v146, v148, v149
	v_mul_f32_e32 v148, 0x42800000, v109
	v_mul_f32_e32 v149, 0x42800000, v113
	v_med3_f32 v148, v148, s101, v158
	v_med3_f32 v149, v149, s101, v158
	v_cvt_pk_fp8_f32 v146, v148, v149 op_sel:[0,0,1]
	v_mov_b32_e32 v147, v159
	v_mul_f32_e32 v148, 0x42800000, v117
	v_mul_f32_e32 v149, 0x42800000, v121
	v_med3_f32 v148, v148, s101, v158
	v_med3_f32 v149, v149, s101, v158
	v_cvt_pk_fp8_f32 v147, v148, v149
	v_mul_f32_e32 v148, 0x42800000, v125
	v_mul_f32_e32 v149, 0x42800000, v129
	v_med3_f32 v148, v148, s101, v158
	v_med3_f32 v149, v149, s101, v158
	v_cvt_pk_fp8_f32 v147, v148, v149 op_sel:[0,0,1]
	ds_write_b64 v163, v[140:141]
	ds_write_b64 v163, v[142:143] offset:64
	ds_write_b64 v163, v[144:145] offset:128
	ds_write_b64 v163, v[146:147] offset:192
	s_waitcnt lgkmcnt(0)
	s_barrier
	ds_read_b128 v[150:153], v164
	ds_read_b128 v[154:157], v164 offset:8192
	s_add_u32 s22, s36, 0x4000
	s_addc_u32 s23, s37, 0
	s_waitcnt lgkmcnt(1)
	global_store_dwordx4 v166, v[150:153], s[36:37]
	s_waitcnt lgkmcnt(0)
	global_store_dwordx4 v166, v[154:157], s[22:23]
	s_barrier
	s_sub_i32 s29, s29, 1
	s_cmp_lg_u32 s29, 0
	s_cbranch_scc1 .Lic_body_ffnup
; #define GAS __attribute__((address_space(1)))
; #define LAS __attribute__((address_space(3)))
; #define LDS_BARRIER() do { asm volatile("s_waitcnt lgkmcnt(0)" ::: "memory"); __builtin_amdgcn_s_barrier(); asm volatile("" ::: "memory"); } while (0)
; __device__ __forceinline__ void conv_load(const float* W, int N, int k0, int n0, int wave, int lane, f32x4 (&r)[8]) {
;     const int n = n0 + 4 * lane; const bool ok = n < N;
;     const float* p = W + (size_t)(k0 + 8 * wave) * N + n;
; #pragma unroll
;     for (int i = 0; i < 8; ++i) r[i] = ok ? __builtin_nontemporal_load((const GAS f32x4*)(p + (size_t)i * N)) : (f32x4){0.f, 0.f, 0.f, 0.f};
; }
; template <class RowMap>
; __device__ __forceinline__ void conv_store_fp8(const f32x4 (&r)[8], unsigned char* WT, int Kbytes, int k0bytes, int n0, const RowMap rm, LAS unsigned char* T, int tid, int wave, int lane) {
;     const int s = 2 * (lane & 3);
; #pragma unroll
;     for (int j = 0; j < 4; ++j) { const unsigned lo = pk4_fp8(r[0][j] * W8_SCALE, r[1][j] * W8_SCALE, r[2][j] * W8_SCALE, r[3][j] * W8_SCALE), hi = pk4_fp8(r[4][j] * W8_SCALE, r[5][j] * W8_SCALE, r[6][j] * W8_SCALE, r[7][j] * W8_SCALE);
;         *(LAS unsigned long long*)(T + (4 * lane + j) * 64 + 8 * (wave ^ s)) = (unsigned long long)lo | ((unsigned long long)hi << 32); }
;     LDS_BARRIER();
;     const int c16 = tid & 3, rr = tid >> 2;
; #pragma unroll
;     for (int q = 0; q < 2; ++q) { const int row = rr + 128 * q; const v4u v = *(const LAS v4u*)(T + row * 64 + 16 * (c16 ^ ((row >> 2) & 3)));
;         const int dr = rm(n0 + row); if (dr >= 0) *(GAS v4u*)(WT + (unsigned)((((dr >> 8) * (Kbytes >> 7) + (k0bytes >> 7)) << 15) + ((dr & 255) << 7) + (k0bytes & 127) + 16 * c16)) = v; }
;     LDS_BARRIER();
; }
	s_add_u32 s4, s4, 0x72000
	s_addc_u32 s5, s5, 0
	s_add_u32 s36, s34, 64
	s_addc_u32 s37, s35, 0
	global_load_dwordx4 v[98:101], v165, s[4:5] nt
	s_add_u32 s4, s4, 0x2000
	s_addc_u32 s5, s5, 0
	global_load_dwordx4 v[102:105], v165, s[4:5] nt
	s_add_u32 s4, s4, 0x2000
	s_addc_u32 s5, s5, 0
	global_load_dwordx4 v[106:109], v165, s[4:5] nt
	s_add_u32 s4, s4, 0x2000
	s_addc_u32 s5, s5, 0
	global_load_dwordx4 v[110:113], v165, s[4:5] nt
	s_add_u32 s4, s4, 0x2000
	s_addc_u32 s5, s5, 0
	global_load_dwordx4 v[114:117], v165, s[4:5] nt
	s_add_u32 s4, s4, 0x2000
	s_addc_u32 s5, s5, 0
	global_load_dwordx4 v[118:121], v165, s[4:5] nt
	s_add_u32 s4, s4, 0x2000
	s_addc_u32 s5, s5, 0
	global_load_dwordx4 v[122:125], v165, s[4:5] nt
	s_add_u32 s4, s4, 0x2000
	s_addc_u32 s5, s5, 0
	global_load_dwordx4 v[126:129], v165, s[4:5] nt
	s_waitcnt vmcnt(24)
	v_mov_b32_e32 v140, v159
	v_mul_f32_e32 v148, 0x42800000, v2
	v_mul_f32_e32 v149, 0x42800000, v6
	v_med3_f32 v148, v148, s101, v158
	v_med3_f32 v149, v149, s101, v158
	v_cvt_pk_fp8_f32 v140, v148, v149
	v_mul_f32_e32 v148, 0x42800000, v10
	v_mul_f32_e32 v149, 0x42800000, v14
	v_med3_f32 v148, v148, s101, v158
	v_med3_f32 v149, v149, s101, v158
	v_cvt_pk_fp8_f32 v140, v148, v149 op_sel:[0,0,1]
	v_mov_b32_e32 v141, v159
	v_mul_f32_e32 v148, 0x42800000, v18
	v_mul_f32_e32 v149, 0x42800000, v22
	v_med3_f32 v148, v148, s101, v158
	v_med3_f32 v149, v149, s101, v158
	v_cvt_pk_fp8_f32 v141, v148, v149
	v_mul_f32_e32 v148, 0x42800000, v26
	v_mul_f32_e32 v149, 0x42800000, v30
	v_med3_f32 v148, v148, s101, v158
	v_med3_f32 v149, v149, s101, v158
	v_cvt_pk_fp8_f32 v141, v148, v149 op_sel:[0,0,1]
	v_mov_b32_e32 v142, v159
	v_mul_f32_e32 v148, 0x42800000, v3
	v_mul_f32_e32 v149, 0x42800000, v7
	v_med3_f32 v148, v148, s101, v158
	v_med3_f32 v149, v149, s101, v158
	v_cvt_pk_fp8_f32 v142, v148, v149
	v_mul_f32_e32 v148, 0x42800000, v11
	v_mul_f32_e32 v149, 0x42800000, v15
	v_med3_f32 v148, v148, s101, v158
	v_med3_f32 v149, v149, s101, v158
	v_cvt_pk_fp8_f32 v142, v148, v149 op_sel:[0,0,1]
	v_mov_b32_e32 v143, v159
	v_mul_f32_e32 v148, 0x42800000, v19
	v_mul_f32_e32 v149, 0x42800000, v23
	v_med3_f32 v148, v148, s101, v158
	v_med3_f32 v149, v149, s101, v158
	v_cvt_pk_fp8_f32 v143, v148, v149
	v_mul_f32_e32 v148, 0x42800000, v27
	v_mul_f32_e32 v149, 0x42800000, v31
	v_med3_f32 v148, v148, s101, v158
	v_med3_f32 v149, v149, s101, v158
	v_cvt_pk_fp8_f32 v143, v148, v149 op_sel:[0,0,1]
	v_mov_b32_e32 v144, v159
	v_mul_f32_e32 v148, 0x42800000, v4
	v_mul_f32_e32 v149, 0x42800000, v8
	v_med3_f32 v148, v148, s101, v158
	v_med3_f32 v149, v149, s101, v158
	v_cvt_pk_fp8_f32 v144, v148, v149
	v_mul_f32_e32 v148, 0x42800000, v12
	v_mul_f32_e32 v149, 0x42800000, v16
	v_med3_f32 v148, v148, s101, v158
	v_med3_f32 v149, v149, s101, v158
	v_cvt_pk_fp8_f32 v144, v148, v149 op_sel:[0,0,1]
	v_mov_b32_e32 v145, v159
	v_mul_f32_e32 v148, 0x42800000, v20
	v_mul_f32_e32 v149, 0x42800000, v24
	v_med3_f32 v148, v148, s101, v158
	v_med3_f32 v149, v149, s101, v158
	v_cvt_pk_fp8_f32 v145, v148, v149
	v_mul_f32_e32 v148, 0x42800000, v28
	v_mul_f32_e32 v149, 0x42800000, v32
	v_med3_f32 v148, v148, s101, v158
	v_med3_f32 v149, v149, s101, v158
	v_cvt_pk_fp8_f32 v145, v148, v149 op_sel:[0,0,1]
	v_mov_b32_e32 v146, v159
	v_mul_f32_e32 v148, 0x42800000, v5
	v_mul_f32_e32 v149, 0x42800000, v9
	v_med3_f32 v148, v148, s101, v158
	v_med3_f32 v149, v149, s101, v158
	v_cvt_pk_fp8_f32 v146, v148, v149
	v_mul_f32_e32 v148, 0x42800000, v13
	v_mul_f32_e32 v149, 0x42800000, v17
	v_med3_f32 v148, v148, s101, v158
	v_med3_f32 v149, v149, s101, v158
	v_cvt_pk_fp8_f32 v146, v148, v149 op_sel:[0,0,1]
	v_mov_b32_e32 v147, v159
	v_mul_f32_e32 v148, 0x42800000, v21
	v_mul_f32_e32 v149, 0x42800000, v25
	v_med3_f32 v148, v148, s101, v158
	v_med3_f32 v149, v149, s101, v158
	v_cvt_pk_fp8_f32 v147, v148, v149
	v_mul_f32_e32 v148, 0x42800000, v29
	v_mul_f32_e32 v149, 0x42800000, v33
	v_med3_f32 v148, v148, s101, v158
	v_med3_f32 v149, v149, s101, v158
	v_cvt_pk_fp8_f32 v147, v148, v149 op_sel:[0,0,1]
	ds_write_b64 v163, v[140:141]
	ds_write_b64 v163, v[142:143] offset:64
	ds_write_b64 v163, v[144:145] offset:128
	ds_write_b64 v163, v[146:147] offset:192
	s_waitcnt lgkmcnt(0)
	s_barrier
	ds_read_b128 v[150:153], v164
	ds_read_b128 v[154:157], v164 offset:8192
	s_add_u32 s22, s30, 0x4000
	s_addc_u32 s23, s31, 0
	s_waitcnt lgkmcnt(1)
	global_store_dwordx4 v166, v[150:153], s[30:31]
	s_waitcnt lgkmcnt(0)
	global_store_dwordx4 v166, v[154:157], s[22:23]
	s_barrier
; #define GAS __attribute__((address_space(1)))
; #define LAS __attribute__((address_space(3)))
; #define LDS_BARRIER() do { asm volatile("s_waitcnt lgkmcnt(0)" ::: "memory"); __builtin_amdgcn_s_barrier(); asm volatile("" ::: "memory"); } while (0)
; __device__ __forceinline__ unsigned pk4_fp8(float a, float b, float c, float d) {
;     a = __builtin_amdgcn_fmed3f(a, -448.f, 448.f); b = __builtin_amdgcn_fmed3f(b, -448.f, 448.f); c = __builtin_amdgcn_fmed3f(c, -448.f, 448.f); d = __builtin_amdgcn_fmed3f(d, -448.f, 448.f);
;     int w = 0; w = __builtin_amdgcn_cvt_pk_fp8_f32(a, b, w, false); w = __builtin_amdgcn_cvt_pk_fp8_f32(c, d, w, true); return (unsigned)w; }
; template <class RowMap>
; __device__ __forceinline__ void conv_store_fp8(const f32x4 (&r)[8], unsigned char* WT, int Kbytes, int k0bytes, int n0, const RowMap rm, LAS unsigned char* T, int tid, int wave, int lane) {
;     const int s = 2 * (lane & 3);
; #pragma unroll
;     for (int j = 0; j < 4; ++j) { const unsigned lo = pk4_fp8(r[0][j] * W8_SCALE, r[1][j] * W8_SCALE, r[2][j] * W8_SCALE, r[3][j] * W8_SCALE), hi = pk4_fp8(r[4][j] * W8_SCALE, r[5][j] * W8_SCALE, r[6][j] * W8_SCALE, r[7][j] * W8_SCALE);
;         *(LAS unsigned long long*)(T + (4 * lane + j) * 64 + 8 * (wave ^ s)) = (unsigned long long)lo | ((unsigned long long)hi << 32); }
;     LDS_BARRIER();
;     const int c16 = tid & 3, rr = tid >> 2;
; #pragma unroll
;     for (int q = 0; q < 2; ++q) { const int row = rr + 128 * q; const v4u v = *(const LAS v4u*)(T + row * 64 + 16 * (c16 ^ ((row >> 2) & 3)));
;         const int dr = rm(n0 + row); if (dr >= 0) *(GAS v4u*)(WT + (unsigned)((((dr >> 8) * (Kbytes >> 7) + (k0bytes >> 7)) << 15) + ((dr & 255) << 7) + (k0bytes & 127) + 16 * c16)) = v; }
;     LDS_BARRIER();
; }
	s_waitcnt vmcnt(22)
	v_mov_b32_e32 v140, v159
	v_mul_f32_e32 v148, 0x42800000, v34
	v_mul_f32_e32 v149, 0x42800000, v38
	v_med3_f32 v148, v148, s101, v158
	v_med3_f32 v149, v149, s101, v158
	v_cvt_pk_fp8_f32 v140, v148, v149
	v_mul_f32_e32 v148, 0x42800000, v42
	v_mul_f32_e32 v149, 0x42800000, v46
	v_med3_f32 v148, v148, s101, v158
	v_med3_f32 v149, v149, s101, v158
	v_cvt_pk_fp8_f32 v140, v148, v149 op_sel:[0,0,1]
	v_mov_b32_e32 v141, v159
	v_mul_f32_e32 v148, 0x42800000, v50
	v_mul_f32_e32 v149, 0x42800000, v54
	v_med3_f32 v148, v148, s101, v158
	v_med3_f32 v149, v149, s101, v158
	v_cvt_pk_fp8_f32 v141, v148, v149
	v_mul_f32_e32 v148, 0x42800000, v58
	v_mul_f32_e32 v149, 0x42800000, v62
	v_med3_f32 v148, v148, s101, v158
	v_med3_f32 v149, v149, s101, v158
	v_cvt_pk_fp8_f32 v141, v148, v149 op_sel:[0,0,1]
	v_mov_b32_e32 v142, v159
	v_mul_f32_e32 v148, 0x42800000, v35
	v_mul_f32_e32 v149, 0x42800000, v39
	v_med3_f32 v148, v148, s101, v158
	v_med3_f32 v149, v149, s101, v158
	v_cvt_pk_fp8_f32 v142, v148, v149
	v_mul_f32_e32 v148, 0x42800000, v43
	v_mul_f32_e32 v149, 0x42800000, v47
	v_med3_f32 v148, v148, s101, v158
	v_med3_f32 v149, v149, s101, v158
	v_cvt_pk_fp8_f32 v142, v148, v149 op_sel:[0,0,1]
	v_mov_b32_e32 v143, v159
	v_mul_f32_e32 v148, 0x42800000, v51
	v_mul_f32_e32 v149, 0x42800000, v55
	v_med3_f32 v148, v148, s101, v158
	v_med3_f32 v149, v149, s101, v158
	v_cvt_pk_fp8_f32 v143, v148, v149
	v_mul_f32_e32 v148, 0x42800000, v59
	v_mul_f32_e32 v149, 0x42800000, v63
	v_med3_f32 v148, v148, s101, v158
	v_med3_f32 v149, v149, s101, v158
	v_cvt_pk_fp8_f32 v143, v148, v149 op_sel:[0,0,1]
	v_mov_b32_e32 v144, v159
	v_mul_f32_e32 v148, 0x42800000, v36
	v_mul_f32_e32 v149, 0x42800000, v40
	v_med3_f32 v148, v148, s101, v158
	v_med3_f32 v149, v149, s101, v158
	v_cvt_pk_fp8_f32 v144, v148, v149
	v_mul_f32_e32 v148, 0x42800000, v44
	v_mul_f32_e32 v149, 0x42800000, v48
	v_med3_f32 v148, v148, s101, v158
	v_med3_f32 v149, v149, s101, v158
	v_cvt_pk_fp8_f32 v144, v148, v149 op_sel:[0,0,1]
	v_mov_b32_e32 v145, v159
	v_mul_f32_e32 v148, 0x42800000, v52
	v_mul_f32_e32 v149, 0x42800000, v56
	v_med3_f32 v148, v148, s101, v158
	v_med3_f32 v149, v149, s101, v158
	v_cvt_pk_fp8_f32 v145, v148, v149
	v_mul_f32_e32 v148, 0x42800000, v60
	v_mul_f32_e32 v149, 0x42800000, v64
	v_med3_f32 v148, v148, s101, v158
	v_med3_f32 v149, v149, s101, v158
	v_cvt_pk_fp8_f32 v145, v148, v149 op_sel:[0,0,1]
	v_mov_b32_e32 v146, v159
	v_mul_f32_e32 v148, 0x42800000, v37
	v_mul_f32_e32 v149, 0x42800000, v41
	v_med3_f32 v148, v148, s101, v158
	v_med3_f32 v149, v149, s101, v158
	v_cvt_pk_fp8_f32 v146, v148, v149
	v_mul_f32_e32 v148, 0x42800000, v45
	v_mul_f32_e32 v149, 0x42800000, v49
	v_med3_f32 v148, v148, s101, v158
	v_med3_f32 v149, v149, s101, v158
	v_cvt_pk_fp8_f32 v146, v148, v149 op_sel:[0,0,1]
	v_mov_b32_e32 v147, v159
	v_mul_f32_e32 v148, 0x42800000, v53
	v_mul_f32_e32 v149, 0x42800000, v57
	v_med3_f32 v148, v148, s101, v158
	v_med3_f32 v149, v149, s101, v158
	v_cvt_pk_fp8_f32 v147, v148, v149
	v_mul_f32_e32 v148, 0x42800000, v61
	v_mul_f32_e32 v149, 0x42800000, v65
	v_med3_f32 v148, v148, s101, v158
	v_med3_f32 v149, v149, s101, v158
	v_cvt_pk_fp8_f32 v147, v148, v149 op_sel:[0,0,1]
	ds_write_b64 v163, v[140:141]
	ds_write_b64 v163, v[142:143] offset:64
	ds_write_b64 v163, v[144:145] offset:128
	ds_write_b64 v163, v[146:147] offset:192
	s_waitcnt lgkmcnt(0)
	s_barrier
	ds_read_b128 v[150:153], v164
	ds_read_b128 v[154:157], v164 offset:8192
	s_add_u32 s22, s32, 0x4000
	s_addc_u32 s23, s33, 0
	s_waitcnt lgkmcnt(1)
	global_store_dwordx4 v166, v[150:153], s[32:33]
	s_waitcnt lgkmcnt(0)
	global_store_dwordx4 v166, v[154:157], s[22:23]
	s_barrier
	s_waitcnt vmcnt(14)
	v_mov_b32_e32 v140, v159
	v_mul_f32_e32 v148, 0x42800000, v66
	v_mul_f32_e32 v149, 0x42800000, v70
	v_med3_f32 v148, v148, s101, v158
	v_med3_f32 v149, v149, s101, v158
	v_cvt_pk_fp8_f32 v140, v148, v149
	v_mul_f32_e32 v148, 0x42800000, v74
	v_mul_f32_e32 v149, 0x42800000, v78
	v_med3_f32 v148, v148, s101, v158
	v_med3_f32 v149, v149, s101, v158
	v_cvt_pk_fp8_f32 v140, v148, v149 op_sel:[0,0,1]
	v_mov_b32_e32 v141, v159
	v_mul_f32_e32 v148, 0x42800000, v82
	v_mul_f32_e32 v149, 0x42800000, v86
	v_med3_f32 v148, v148, s101, v158
	v_med3_f32 v149, v149, s101, v158
	v_cvt_pk_fp8_f32 v141, v148, v149
	v_mul_f32_e32 v148, 0x42800000, v90
	v_mul_f32_e32 v149, 0x42800000, v94
	v_med3_f32 v148, v148, s101, v158
	v_med3_f32 v149, v149, s101, v158
	v_cvt_pk_fp8_f32 v141, v148, v149 op_sel:[0,0,1]
	v_mov_b32_e32 v142, v159
	v_mul_f32_e32 v148, 0x42800000, v67
	v_mul_f32_e32 v149, 0x42800000, v71
	v_med3_f32 v148, v148, s101, v158
	v_med3_f32 v149, v149, s101, v158
	v_cvt_pk_fp8_f32 v142, v148, v149
	v_mul_f32_e32 v148, 0x42800000, v75
	v_mul_f32_e32 v149, 0x42800000, v79
	v_med3_f32 v148, v148, s101, v158
	v_med3_f32 v149, v149, s101, v158
	v_cvt_pk_fp8_f32 v142, v148, v149 op_sel:[0,0,1]
	v_mov_b32_e32 v143, v159
	v_mul_f32_e32 v148, 0x42800000, v83
	v_mul_f32_e32 v149, 0x42800000, v87
	v_med3_f32 v148, v148, s101, v158
	v_med3_f32 v149, v149, s101, v158
	v_cvt_pk_fp8_f32 v143, v148, v149
	v_mul_f32_e32 v148, 0x42800000, v91
	v_mul_f32_e32 v149, 0x42800000, v95
	v_med3_f32 v148, v148, s101, v158
	v_med3_f32 v149, v149, s101, v158
	v_cvt_pk_fp8_f32 v143, v148, v149 op_sel:[0,0,1]
	v_mov_b32_e32 v144, v159
	v_mul_f32_e32 v148, 0x42800000, v68
	v_mul_f32_e32 v149, 0x42800000, v72
	v_med3_f32 v148, v148, s101, v158
	v_med3_f32 v149, v149, s101, v158
	v_cvt_pk_fp8_f32 v144, v148, v149
	v_mul_f32_e32 v148, 0x42800000, v76
	v_mul_f32_e32 v149, 0x42800000, v80
	v_med3_f32 v148, v148, s101, v158
	v_med3_f32 v149, v149, s101, v158
; #define GAS __attribute__((address_space(1)))
; #define LAS __attribute__((address_space(3)))
; #define LDS_BARRIER() do { asm volatile("s_waitcnt lgkmcnt(0)" ::: "memory"); __builtin_amdgcn_s_barrier(); asm volatile("" ::: "memory"); } while (0)
; __device__ __forceinline__ unsigned pk4_fp8(float a, float b, float c, float d) {
;     a = __builtin_amdgcn_fmed3f(a, -448.f, 448.f); b = __builtin_amdgcn_fmed3f(b, -448.f, 448.f); c = __builtin_amdgcn_fmed3f(c, -448.f, 448.f); d = __builtin_amdgcn_fmed3f(d, -448.f, 448.f);
;     int w = 0; w = __builtin_amdgcn_cvt_pk_fp8_f32(a, b, w, false); w = __builtin_amdgcn_cvt_pk_fp8_f32(c, d, w, true); return (unsigned)w; }
; template <class RowMap>
; __device__ __forceinline__ void conv_store_fp8(const f32x4 (&r)[8], unsigned char* WT, int Kbytes, int k0bytes, int n0, const RowMap rm, LAS unsigned char* T, int tid, int wave, int lane) {
;     const int s = 2 * (lane & 3);
; #pragma unroll
;     for (int j = 0; j < 4; ++j) { const unsigned lo = pk4_fp8(r[0][j] * W8_SCALE, r[1][j] * W8_SCALE, r[2][j] * W8_SCALE, r[3][j] * W8_SCALE), hi = pk4_fp8(r[4][j] * W8_SCALE, r[5][j] * W8_SCALE, r[6][j] * W8_SCALE, r[7][j] * W8_SCALE);
;         *(LAS unsigned long long*)(T + (4 * lane + j) * 64 + 8 * (wave ^ s)) = (unsigned long long)lo | ((unsigned long long)hi << 32); }
;     LDS_BARRIER();
;     const int c16 = tid & 3, rr = tid >> 2;
; #pragma unroll
;     for (int q = 0; q < 2; ++q) { const int row = rr + 128 * q; const v4u v = *(const LAS v4u*)(T + row * 64 + 16 * (c16 ^ ((row >> 2) & 3)));
;         const int dr = rm(n0 + row); if (dr >= 0) *(GAS v4u*)(WT + (unsigned)((((dr >> 8) * (Kbytes >> 7) + (k0bytes >> 7)) << 15) + ((dr & 255) << 7) + (k0bytes & 127) + 16 * c16)) = v; }
;     LDS_BARRIER();
; }
	v_cvt_pk_fp8_f32 v144, v148, v149 op_sel:[0,0,1]
	v_mov_b32_e32 v145, v159
	v_mul_f32_e32 v148, 0x42800000, v84
	v_mul_f32_e32 v149, 0x42800000, v88
	v_med3_f32 v148, v148, s101, v158
	v_med3_f32 v149, v149, s101, v158
	v_cvt_pk_fp8_f32 v145, v148, v149
	v_mul_f32_e32 v148, 0x42800000, v92
	v_mul_f32_e32 v149, 0x42800000, v96
	v_med3_f32 v148, v148, s101, v158
	v_med3_f32 v149, v149, s101, v158
	v_cvt_pk_fp8_f32 v145, v148, v149 op_sel:[0,0,1]
	v_mov_b32_e32 v146, v159
	v_mul_f32_e32 v148, 0x42800000, v69
	v_mul_f32_e32 v149, 0x42800000, v73
	v_med3_f32 v148, v148, s101, v158
	v_med3_f32 v149, v149, s101, v158
	v_cvt_pk_fp8_f32 v146, v148, v149
	v_mul_f32_e32 v148, 0x42800000, v77
	v_mul_f32_e32 v149, 0x42800000, v81
	v_med3_f32 v148, v148, s101, v158
	v_med3_f32 v149, v149, s101, v158
	v_cvt_pk_fp8_f32 v146, v148, v149 op_sel:[0,0,1]
	v_mov_b32_e32 v147, v159
	v_mul_f32_e32 v148, 0x42800000, v85
	v_mul_f32_e32 v149, 0x42800000, v89
	v_med3_f32 v148, v148, s101, v158
	v_med3_f32 v149, v149, s101, v158
	v_cvt_pk_fp8_f32 v147, v148, v149
	v_mul_f32_e32 v148, 0x42800000, v93
	v_mul_f32_e32 v149, 0x42800000, v97
	v_med3_f32 v148, v148, s101, v158
	v_med3_f32 v149, v149, s101, v158
	v_cvt_pk_fp8_f32 v147, v148, v149 op_sel:[0,0,1]
	ds_write_b64 v163, v[140:141]
	ds_write_b64 v163, v[142:143] offset:64
	ds_write_b64 v163, v[144:145] offset:128
	ds_write_b64 v163, v[146:147] offset:192
	s_waitcnt lgkmcnt(0)
	s_barrier
	ds_read_b128 v[150:153], v164
	ds_read_b128 v[154:157], v164 offset:8192
	s_add_u32 s22, s34, 0x4000
	s_addc_u32 s23, s35, 0
	s_waitcnt lgkmcnt(1)
	global_store_dwordx4 v166, v[150:153], s[34:35]
	s_waitcnt lgkmcnt(0)
	global_store_dwordx4 v166, v[154:157], s[22:23]
	s_barrier
	s_waitcnt vmcnt(6)
	v_mov_b32_e32 v140, v159
	v_mul_f32_e32 v148, 0x42800000, v98
	v_mul_f32_e32 v149, 0x42800000, v102
	v_med3_f32 v148, v148, s101, v158
	v_med3_f32 v149, v149, s101, v158
	v_cvt_pk_fp8_f32 v140, v148, v149
	v_mul_f32_e32 v148, 0x42800000, v106
	v_mul_f32_e32 v149, 0x42800000, v110
	v_med3_f32 v148, v148, s101, v158
	v_med3_f32 v149, v149, s101, v158
	v_cvt_pk_fp8_f32 v140, v148, v149 op_sel:[0,0,1]
	v_mov_b32_e32 v141, v159
	v_mul_f32_e32 v148, 0x42800000, v114
	v_mul_f32_e32 v149, 0x42800000, v118
	v_med3_f32 v148, v148, s101, v158
	v_med3_f32 v149, v149, s101, v158
	v_cvt_pk_fp8_f32 v141, v148, v149
	v_mul_f32_e32 v148, 0x42800000, v122
	v_mul_f32_e32 v149, 0x42800000, v126
	v_med3_f32 v148, v148, s101, v158
	v_med3_f32 v149, v149, s101, v158
	v_cvt_pk_fp8_f32 v141, v148, v149 op_sel:[0,0,1]
	v_mov_b32_e32 v142, v159
	v_mul_f32_e32 v148, 0x42800000, v99
	v_mul_f32_e32 v149, 0x42800000, v103
	v_med3_f32 v148, v148, s101, v158
	v_med3_f32 v149, v149, s101, v158
	v_cvt_pk_fp8_f32 v142, v148, v149
	v_mul_f32_e32 v148, 0x42800000, v107
	v_mul_f32_e32 v149, 0x42800000, v111
	v_med3_f32 v148, v148, s101, v158
	v_med3_f32 v149, v149, s101, v158
	v_cvt_pk_fp8_f32 v142, v148, v149 op_sel:[0,0,1]
	v_mov_b32_e32 v143, v159
	v_mul_f32_e32 v148, 0x42800000, v115
	v_mul_f32_e32 v149, 0x42800000, v119
	v_med3_f32 v148, v148, s101, v158
	v_med3_f32 v149, v149, s101, v158
	v_cvt_pk_fp8_f32 v143, v148, v149
	v_mul_f32_e32 v148, 0x42800000, v123
	v_mul_f32_e32 v149, 0x42800000, v127
	v_med3_f32 v148, v148, s101, v158
	v_med3_f32 v149, v149, s101, v158
	v_cvt_pk_fp8_f32 v143, v148, v149 op_sel:[0,0,1]
	v_mov_b32_e32 v144, v159
	v_mul_f32_e32 v148, 0x42800000, v100
	v_mul_f32_e32 v149, 0x42800000, v104
	v_med3_f32 v148, v148, s101, v158
	v_med3_f32 v149, v149, s101, v158
	v_cvt_pk_fp8_f32 v144, v148, v149
	v_mul_f32_e32 v148, 0x42800000, v108
	v_mul_f32_e32 v149, 0x42800000, v112
	v_med3_f32 v148, v148, s101, v158
	v_med3_f32 v149, v149, s101, v158
	v_cvt_pk_fp8_f32 v144, v148, v149 op_sel:[0,0,1]
	v_mov_b32_e32 v145, v159
	v_mul_f32_e32 v148, 0x42800000, v116
	v_mul_f32_e32 v149, 0x42800000, v120
	v_med3_f32 v148, v148, s101, v158
	v_med3_f32 v149, v149, s101, v158
	v_cvt_pk_fp8_f32 v145, v148, v149
	v_mul_f32_e32 v148, 0x42800000, v124
	v_mul_f32_e32 v149, 0x42800000, v128
	v_med3_f32 v148, v148, s101, v158
	v_med3_f32 v149, v149, s101, v158
	v_cvt_pk_fp8_f32 v145, v148, v149 op_sel:[0,0,1]
	v_mov_b32_e32 v146, v159
	v_mul_f32_e32 v148, 0x42800000, v101
	v_mul_f32_e32 v149, 0x42800000, v105
	v_med3_f32 v148, v148, s101, v158
	v_med3_f32 v149, v149, s101, v158
	v_cvt_pk_fp8_f32 v146, v148, v149
	v_mul_f32_e32 v148, 0x42800000, v109
	v_mul_f32_e32 v149, 0x42800000, v113
	v_med3_f32 v148, v148, s101, v158
	v_med3_f32 v149, v149, s101, v158
	v_cvt_pk_fp8_f32 v146, v148, v149 op_sel:[0,0,1]
	v_mov_b32_e32 v147, v159
	v_mul_f32_e32 v148, 0x42800000, v117
	v_mul_f32_e32 v149, 0x42800000, v121
	v_med3_f32 v148, v148, s101, v158
	v_med3_f32 v149, v149, s101, v158
	v_cvt_pk_fp8_f32 v147, v148, v149
	v_mul_f32_e32 v148, 0x42800000, v125
	v_mul_f32_e32 v149, 0x42800000, v129
	v_med3_f32 v148, v148, s101, v158
	v_med3_f32 v149, v149, s101, v158
	v_cvt_pk_fp8_f32 v147, v148, v149 op_sel:[0,0,1]
	ds_write_b64 v163, v[140:141]
	ds_write_b64 v163, v[142:143] offset:64
	ds_write_b64 v163, v[144:145] offset:128
	ds_write_b64 v163, v[146:147] offset:192
	s_waitcnt lgkmcnt(0)
	s_barrier
	ds_read_b128 v[150:153], v164
	ds_read_b128 v[154:157], v164 offset:8192
	s_add_u32 s22, s36, 0x4000
	s_addc_u32 s23, s37, 0
	s_waitcnt lgkmcnt(1)
	global_store_dwordx4 v166, v[150:153], s[36:37]
	s_waitcnt lgkmcnt(0)
	global_store_dwordx4 v166, v[154:157], s[22:23]
	s_barrier
	v_readlane_b32 s4, v255, 25
	v_readlane_b32 s5, v255, 26
	v_readlane_b32 s6, v255, 27
	v_readlane_b32 s7, v255, 28
	v_readlane_b32 s8, v255, 29
	v_readlane_b32 s9, v255, 30
	v_readlane_b32 s10, v255, 31
	v_readlane_b32 s11, v255, 32
	v_readlane_b32 s12, v255, 33
	v_readlane_b32 s13, v255, 34
	v_readlane_b32 s14, v255, 35
	v_readlane_b32 s15, v255, 36
	v_readlane_b32 s16, v255, 37
	v_readlane_b32 s17, v255, 38
	v_readlane_b32 s18, v255, 39
	v_readlane_b32 s19, v255, 40
	v_readlane_b32 s20, v255, 41
	v_readlane_b32 s21, v255, 42
	v_readlane_b32 s22, v255, 43
	v_readlane_b32 s23, v255, 44
	v_readlane_b32 s24, v255, 45
	v_readlane_b32 s25, v255, 46
	v_readlane_b32 s26, v255, 47
	v_readlane_b32 s27, v255, 48
	v_readlane_b32 s28, v255, 49
	v_readlane_b32 s29, v255, 50
	v_readlane_b32 s30, v255, 51
	v_readlane_b32 s31, v255, 52
	v_readlane_b32 s32, v255, 53
	v_readlane_b32 s33, v255, 54
	v_readlane_b32 s34, v255, 55
	v_readlane_b32 s35, v255, 56
	v_readlane_b32 s36, v255, 57
	v_readlane_b32 s37, v255, 58
	v_readlane_b32 s38, v255, 59
	v_readlane_b32 s39, v255, 60
	s_nop 3
